# forget-weight gather in one round trip; P3 and P4 epilogue loads issued up front; MFMA order within GEMM blocks changed to share an operand with the previous MFMA
# baseline (speedup 1.0000x reference)
.LBB0_114:
	ds_read_b128 v[130:133], v220
	ds_read_b128 v[134:137], v220 offset:1024
	ds_read_b128 v[138:141], v220 offset:2048
	ds_read_b128 v[142:145], v220 offset:3072
	ds_read_b128 v[146:149], v221
	ds_read_b128 v[150:153], v221 offset:1024
	ds_read_b128 v[154:157], v221 offset:2048
	ds_read_b128 v[158:161], v221 offset:3072
	s_add_i32 s46, s64, 0xfff80080
	s_cmp_eq_u32 s84, 28
	s_cselect_b32 s87, s62, s46
	s_cselect_b32 s86, s63, s65
	s_or_b32 s85, s87, 0x80
	s_mov_b32 m0, s93
	ds_read_b128 v[162:165], v222
	ds_read_b128 v[166:169], v222 offset:1024
	ds_read_b128 v[170:173], v222 offset:2048
	ds_read_b128 v[174:177], v222 offset:3072
	ds_read_b128 v[178:181], v222 offset:4096
	ds_read_b128 v[182:185], v222 offset:5120
	ds_read_b128 v[186:189], v222 offset:6144
	ds_read_b128 v[212:215], v222 offset:7168
	buffer_load_dwordx4 v1, s[40:43], s64 offen lds
	s_mov_b32 m0, s94
	s_nop 0
	buffer_load_dwordx4 v216, s[40:43], s64 offen lds
	s_waitcnt vmcnt(8)
	s_waitcnt lgkmcnt(0)
	s_barrier
	s_setprio 1
	s_waitcnt lgkmcnt(7)
	v_mfma_f32_16x16x32_bf16 v[126:129], v[130:133], v[162:165], v[126:129]
	v_mfma_f32_16x16x32_bf16 v[122:125], v[138:141], v[162:165], v[122:125]
	s_waitcnt lgkmcnt(5)
	v_mfma_f32_16x16x32_bf16 v[106:109], v[138:141], v[170:173], v[106:109]
	v_mfma_f32_16x16x32_bf16 v[114:117], v[130:133], v[170:173], v[114:117]
	s_waitcnt lgkmcnt(3)
	v_mfma_f32_16x16x32_bf16 v[102:105], v[130:133], v[178:181], v[102:105]
	v_mfma_f32_16x16x32_bf16 v[94:97], v[138:141], v[178:181], v[94:97]
	s_waitcnt lgkmcnt(1)
	v_mfma_f32_16x16x32_bf16 v[78:81], v[138:141], v[186:189], v[78:81]
	v_mfma_f32_16x16x32_bf16 v[86:89], v[130:133], v[186:189], v[86:89]
	v_mfma_f32_16x16x32_bf16 v[126:129], v[134:137], v[166:169], v[126:129]
	v_mfma_f32_16x16x32_bf16 v[122:125], v[142:145], v[166:169], v[122:125]
	v_mfma_f32_16x16x32_bf16 v[106:109], v[142:145], v[174:177], v[106:109]
	v_mfma_f32_16x16x32_bf16 v[114:117], v[134:137], v[174:177], v[114:117]
	v_mfma_f32_16x16x32_bf16 v[102:105], v[134:137], v[182:185], v[102:105]
	v_mfma_f32_16x16x32_bf16 v[94:97], v[142:145], v[182:185], v[94:97]
	s_waitcnt lgkmcnt(0)
	v_mfma_f32_16x16x32_bf16 v[78:81], v[142:145], v[212:215], v[78:81]
	v_mfma_f32_16x16x32_bf16 v[86:89], v[134:137], v[212:215], v[86:89]
	s_setprio 0
	s_setprio 1
	v_mfma_f32_16x16x32_bf16 v[118:121], v[146:149], v[162:165], v[118:121]
	v_mfma_f32_16x16x32_bf16 v[110:113], v[154:157], v[162:165], v[110:113]
	v_mfma_f32_16x16x32_bf16 v[90:93], v[154:157], v[170:173], v[90:93]
	v_mfma_f32_16x16x32_bf16 v[98:101], v[146:149], v[170:173], v[98:101]
	v_mfma_f32_16x16x32_bf16 v[82:85], v[146:149], v[178:181], v[82:85]
	v_mfma_f32_16x16x32_bf16 v[74:77], v[154:157], v[178:181], v[74:77]
	v_mfma_f32_16x16x32_bf16 v[66:69], v[154:157], v[186:189], v[66:69]
	v_mfma_f32_16x16x32_bf16 v[70:73], v[146:149], v[186:189], v[70:73]
	v_mfma_f32_16x16x32_bf16 v[118:121], v[150:153], v[166:169], v[118:121]
	v_mfma_f32_16x16x32_bf16 v[110:113], v[158:161], v[166:169], v[110:113]
	v_mfma_f32_16x16x32_bf16 v[90:93], v[158:161], v[174:177], v[90:93]
	v_mfma_f32_16x16x32_bf16 v[98:101], v[150:153], v[174:177], v[98:101]
	v_mfma_f32_16x16x32_bf16 v[82:85], v[150:153], v[182:185], v[82:85]
	v_mfma_f32_16x16x32_bf16 v[74:77], v[158:161], v[182:185], v[74:77]
	v_mfma_f32_16x16x32_bf16 v[66:69], v[158:161], v[212:215], v[66:69]
	v_mfma_f32_16x16x32_bf16 v[70:73], v[150:153], v[212:215], v[70:73]
	s_setprio 0
	s_barrier
	s_mov_b32 m0, s69
	s_mov_b32 s46, s42
	s_mov_b32 s47, s43
	ds_read_b128 v[162:165], v222 offset:16384
	ds_read_b128 v[166:169], v222 offset:17408
	ds_read_b128 v[170:173], v222 offset:18432
	ds_read_b128 v[174:177], v222 offset:19456
	ds_read_b128 v[178:181], v222 offset:20480
	ds_read_b128 v[182:185], v222 offset:21504
	ds_read_b128 v[186:189], v222 offset:22528
	ds_read_b128 v[212:215], v222 offset:23552
	buffer_load_dwordx4 v191, s[44:47], s86 offen lds
	s_mov_b32 m0, s70
	s_add_i32 s88, s86, 0x80000
	buffer_load_dwordx4 v217, s[44:47], s86 offen lds
	s_mov_b32 m0, s71
	s_nop 0
	buffer_load_dwordx4 v191, s[44:47], s88 offen lds
	s_mov_b32 m0, s72
	s_nop 0
	buffer_load_dwordx4 v217, s[44:47], s88 offen lds
	s_mov_b32 m0, s68
	s_nop 0
	buffer_load_dwordx4 v1, s[40:43], s87 offen lds
	s_mov_b32 m0, s73
	s_nop 0
	buffer_load_dwordx4 v216, s[40:43], s87 offen lds
	s_waitcnt vmcnt(8)
	s_waitcnt lgkmcnt(0)
	s_barrier
	s_setprio 1
	s_waitcnt lgkmcnt(7)
	v_mfma_f32_16x16x32_bf16 v[62:65], v[130:133], v[162:165], v[62:65]
	v_mfma_f32_16x16x32_bf16 v[58:61], v[138:141], v[162:165], v[58:61]
	s_waitcnt lgkmcnt(5)
	v_mfma_f32_16x16x32_bf16 v[46:49], v[138:141], v[170:173], v[46:49]
	v_mfma_f32_16x16x32_bf16 v[54:57], v[130:133], v[170:173], v[54:57]
	s_waitcnt lgkmcnt(3)
	v_mfma_f32_16x16x32_bf16 v[38:41], v[130:133], v[178:181], v[38:41]
	v_mfma_f32_16x16x32_bf16 v[30:33], v[138:141], v[178:181], v[30:33]
	s_waitcnt lgkmcnt(1)
	v_mfma_f32_16x16x32_bf16 v[14:17], v[138:141], v[186:189], v[14:17]
	v_mfma_f32_16x16x32_bf16 v[22:25], v[130:133], v[186:189], v[22:25]
	v_mfma_f32_16x16x32_bf16 v[62:65], v[134:137], v[166:169], v[62:65]
	v_mfma_f32_16x16x32_bf16 v[58:61], v[142:145], v[166:169], v[58:61]
	v_mfma_f32_16x16x32_bf16 v[46:49], v[142:145], v[174:177], v[46:49]
	v_mfma_f32_16x16x32_bf16 v[54:57], v[134:137], v[174:177], v[54:57]
	v_mfma_f32_16x16x32_bf16 v[38:41], v[134:137], v[182:185], v[38:41]
	v_mfma_f32_16x16x32_bf16 v[30:33], v[142:145], v[182:185], v[30:33]
	s_waitcnt lgkmcnt(0)
	v_mfma_f32_16x16x32_bf16 v[14:17], v[142:145], v[212:215], v[14:17]
	v_mfma_f32_16x16x32_bf16 v[22:25], v[134:137], v[212:215], v[22:25]
	s_setprio 0
	s_setprio 1
	v_mfma_f32_16x16x32_bf16 v[50:53], v[146:149], v[162:165], v[50:53]
	v_mfma_f32_16x16x32_bf16 v[42:45], v[154:157], v[162:165], v[42:45]
	v_mfma_f32_16x16x32_bf16 v[26:29], v[154:157], v[170:173], v[26:29]
	v_mfma_f32_16x16x32_bf16 v[34:37], v[146:149], v[170:173], v[34:37]
	v_mfma_f32_16x16x32_bf16 v[18:21], v[146:149], v[178:181], v[18:21]
	v_mfma_f32_16x16x32_bf16 v[10:13], v[154:157], v[178:181], v[10:13]
	v_mfma_f32_16x16x32_bf16 v[2:5], v[154:157], v[186:189], v[2:5]
	v_mfma_f32_16x16x32_bf16 v[6:9], v[146:149], v[186:189], v[6:9]
	v_mfma_f32_16x16x32_bf16 v[50:53], v[150:153], v[166:169], v[50:53]
	v_mfma_f32_16x16x32_bf16 v[42:45], v[158:161], v[166:169], v[42:45]
	v_mfma_f32_16x16x32_bf16 v[26:29], v[158:161], v[174:177], v[26:29]
	v_mfma_f32_16x16x32_bf16 v[34:37], v[150:153], v[174:177], v[34:37]
	v_mfma_f32_16x16x32_bf16 v[18:21], v[150:153], v[182:185], v[18:21]
	v_mfma_f32_16x16x32_bf16 v[10:13], v[158:161], v[182:185], v[10:13]
	v_mfma_f32_16x16x32_bf16 v[2:5], v[158:161], v[212:215], v[2:5]
	v_mfma_f32_16x16x32_bf16 v[6:9], v[150:153], v[212:215], v[6:9]
	s_setprio 0
	s_barrier
	ds_read_b128 v[130:133], v223
	ds_read_b128 v[134:137], v223 offset:1024
	ds_read_b128 v[138:141], v223 offset:2048
	ds_read_b128 v[142:145], v223 offset:3072
	ds_read_b128 v[146:149], v224
	ds_read_b128 v[150:153], v224 offset:1024
	ds_read_b128 v[154:157], v224 offset:2048
	ds_read_b128 v[158:161], v224 offset:3072
	s_add_i32 s87, s87, 0x80000
	s_mov_b32 m0, s74
	ds_read_b128 v[162:165], v222 offset:32768
	ds_read_b128 v[166:169], v222 offset:33792
	ds_read_b128 v[170:173], v222 offset:34816
	ds_read_b128 v[174:177], v222 offset:35840
	ds_read_b128 v[178:181], v222 offset:36864
	ds_read_b128 v[182:185], v222 offset:37888
	ds_read_b128 v[186:189], v222 offset:38912
	ds_read_b128 v[212:215], v222 offset:39936
	buffer_load_dwordx4 v1, s[40:43], s87 offen lds
	s_mov_b32 m0, s75
	s_nop 0
	buffer_load_dwordx4 v216, s[40:43], s87 offen lds
	s_waitcnt vmcnt(8)
	s_waitcnt lgkmcnt(0)
	s_barrier
	s_setprio 1
	s_waitcnt lgkmcnt(7)
	v_mfma_f32_16x16x32_bf16 v[126:129], v[130:133], v[162:165], v[126:129]
	v_mfma_f32_16x16x32_bf16 v[122:125], v[138:141], v[162:165], v[122:125]
	s_waitcnt lgkmcnt(5)
	v_mfma_f32_16x16x32_bf16 v[106:109], v[138:141], v[170:173], v[106:109]
	v_mfma_f32_16x16x32_bf16 v[114:117], v[130:133], v[170:173], v[114:117]
	s_waitcnt lgkmcnt(3)
	v_mfma_f32_16x16x32_bf16 v[102:105], v[130:133], v[178:181], v[102:105]
	v_mfma_f32_16x16x32_bf16 v[94:97], v[138:141], v[178:181], v[94:97]
	s_waitcnt lgkmcnt(1)
	v_mfma_f32_16x16x32_bf16 v[78:81], v[138:141], v[186:189], v[78:81]
	v_mfma_f32_16x16x32_bf16 v[86:89], v[130:133], v[186:189], v[86:89]
	v_mfma_f32_16x16x32_bf16 v[126:129], v[134:137], v[166:169], v[126:129]
	v_mfma_f32_16x16x32_bf16 v[122:125], v[142:145], v[166:169], v[122:125]
	v_mfma_f32_16x16x32_bf16 v[106:109], v[142:145], v[174:177], v[106:109]
	v_mfma_f32_16x16x32_bf16 v[114:117], v[134:137], v[174:177], v[114:117]
	v_mfma_f32_16x16x32_bf16 v[102:105], v[134:137], v[182:185], v[102:105]
	v_mfma_f32_16x16x32_bf16 v[94:97], v[142:145], v[182:185], v[94:97]
	s_waitcnt lgkmcnt(0)
	v_mfma_f32_16x16x32_bf16 v[78:81], v[142:145], v[212:215], v[78:81]
	v_mfma_f32_16x16x32_bf16 v[86:89], v[134:137], v[212:215], v[86:89]
	s_setprio 0
	s_setprio 1
	v_mfma_f32_16x16x32_bf16 v[118:121], v[146:149], v[162:165], v[118:121]
	v_mfma_f32_16x16x32_bf16 v[110:113], v[154:157], v[162:165], v[110:113]
	v_mfma_f32_16x16x32_bf16 v[90:93], v[154:157], v[170:173], v[90:93]
	v_mfma_f32_16x16x32_bf16 v[98:101], v[146:149], v[170:173], v[98:101]
	v_mfma_f32_16x16x32_bf16 v[82:85], v[146:149], v[178:181], v[82:85]
	v_mfma_f32_16x16x32_bf16 v[74:77], v[154:157], v[178:181], v[74:77]
	v_mfma_f32_16x16x32_bf16 v[66:69], v[154:157], v[186:189], v[66:69]
	v_mfma_f32_16x16x32_bf16 v[70:73], v[146:149], v[186:189], v[70:73]
	v_mfma_f32_16x16x32_bf16 v[118:121], v[150:153], v[166:169], v[118:121]
	v_mfma_f32_16x16x32_bf16 v[110:113], v[158:161], v[166:169], v[110:113]
	v_mfma_f32_16x16x32_bf16 v[90:93], v[158:161], v[174:177], v[90:93]
	v_mfma_f32_16x16x32_bf16 v[98:101], v[150:153], v[174:177], v[98:101]
	v_mfma_f32_16x16x32_bf16 v[82:85], v[150:153], v[182:185], v[82:85]
	v_mfma_f32_16x16x32_bf16 v[74:77], v[158:161], v[182:185], v[74:77]
	v_mfma_f32_16x16x32_bf16 v[66:69], v[158:161], v[212:215], v[66:69]
	v_mfma_f32_16x16x32_bf16 v[70:73], v[150:153], v[212:215], v[70:73]
	s_setprio 0
	s_barrier
	s_mov_b32 m0, s79
	s_or_b32 s87, s86, 0x80
	ds_read_b128 v[162:165], v222 offset:49152
	ds_read_b128 v[166:169], v222 offset:50176
	ds_read_b128 v[170:173], v222 offset:51200
	ds_read_b128 v[174:177], v222 offset:52224
	ds_read_b128 v[178:181], v222 offset:53248
	ds_read_b128 v[182:185], v222 offset:54272
	ds_read_b128 v[186:189], v222 offset:55296
	ds_read_b128 v[212:215], v222 offset:56320
	buffer_load_dwordx4 v191, s[44:47], s87 offen lds
	s_mov_b32 m0, s80
	s_add_i32 s86, s86, 0x80080
	buffer_load_dwordx4 v217, s[44:47], s87 offen lds
	s_mov_b32 m0, s83
	s_nop 0
	buffer_load_dwordx4 v191, s[44:47], s86 offen lds
	s_mov_b32 m0, s92
	s_nop 0
	buffer_load_dwordx4 v217, s[44:47], s86 offen lds
	s_mov_b32 m0, s81
	s_nop 0
	buffer_load_dwordx4 v1, s[40:43], s85 offen lds
	s_mov_b32 m0, s82
	s_nop 0
	buffer_load_dwordx4 v216, s[40:43], s85 offen lds
	s_waitcnt vmcnt(8)
	s_waitcnt lgkmcnt(0)
	s_barrier
	s_setprio 1
	s_waitcnt lgkmcnt(7)
	v_mfma_f32_16x16x32_bf16 v[62:65], v[130:133], v[162:165], v[62:65]
	v_mfma_f32_16x16x32_bf16 v[58:61], v[138:141], v[162:165], v[58:61]
	s_waitcnt lgkmcnt(5)
	v_mfma_f32_16x16x32_bf16 v[46:49], v[138:141], v[170:173], v[46:49]
	v_mfma_f32_16x16x32_bf16 v[54:57], v[130:133], v[170:173], v[54:57]
	s_waitcnt lgkmcnt(3)
	v_mfma_f32_16x16x32_bf16 v[38:41], v[130:133], v[178:181], v[38:41]
	v_mfma_f32_16x16x32_bf16 v[30:33], v[138:141], v[178:181], v[30:33]
	s_waitcnt lgkmcnt(1)
	v_mfma_f32_16x16x32_bf16 v[14:17], v[138:141], v[186:189], v[14:17]
	v_mfma_f32_16x16x32_bf16 v[22:25], v[130:133], v[186:189], v[22:25]
	v_mfma_f32_16x16x32_bf16 v[62:65], v[134:137], v[166:169], v[62:65]
	v_mfma_f32_16x16x32_bf16 v[58:61], v[142:145], v[166:169], v[58:61]
	v_mfma_f32_16x16x32_bf16 v[46:49], v[142:145], v[174:177], v[46:49]
	v_mfma_f32_16x16x32_bf16 v[54:57], v[134:137], v[174:177], v[54:57]
	v_mfma_f32_16x16x32_bf16 v[38:41], v[134:137], v[182:185], v[38:41]
	v_mfma_f32_16x16x32_bf16 v[30:33], v[142:145], v[182:185], v[30:33]
	s_waitcnt lgkmcnt(0)
	v_mfma_f32_16x16x32_bf16 v[14:17], v[142:145], v[212:215], v[14:17]
	v_mfma_f32_16x16x32_bf16 v[22:25], v[134:137], v[212:215], v[22:25]
	s_setprio 0
	s_setprio 1
	v_mfma_f32_16x16x32_bf16 v[50:53], v[146:149], v[162:165], v[50:53]
	v_mfma_f32_16x16x32_bf16 v[42:45], v[154:157], v[162:165], v[42:45]
	v_mfma_f32_16x16x32_bf16 v[26:29], v[154:157], v[170:173], v[26:29]
	v_mfma_f32_16x16x32_bf16 v[34:37], v[146:149], v[170:173], v[34:37]
	v_mfma_f32_16x16x32_bf16 v[18:21], v[146:149], v[178:181], v[18:21]
	v_mfma_f32_16x16x32_bf16 v[10:13], v[154:157], v[178:181], v[10:13]
	v_mfma_f32_16x16x32_bf16 v[2:5], v[154:157], v[186:189], v[2:5]
	v_mfma_f32_16x16x32_bf16 v[6:9], v[146:149], v[186:189], v[6:9]
	v_mfma_f32_16x16x32_bf16 v[50:53], v[150:153], v[166:169], v[50:53]
	v_mfma_f32_16x16x32_bf16 v[42:45], v[158:161], v[166:169], v[42:45]
	v_mfma_f32_16x16x32_bf16 v[26:29], v[158:161], v[174:177], v[26:29]
	v_mfma_f32_16x16x32_bf16 v[34:37], v[150:153], v[174:177], v[34:37]
	v_mfma_f32_16x16x32_bf16 v[18:21], v[150:153], v[182:185], v[18:21]
	v_mfma_f32_16x16x32_bf16 v[10:13], v[158:161], v[182:185], v[10:13]
	v_mfma_f32_16x16x32_bf16 v[2:5], v[158:161], v[212:215], v[2:5]
	v_mfma_f32_16x16x32_bf16 v[6:9], v[150:153], v[212:215], v[6:9]
	s_setprio 0
	s_barrier
	s_add_i32 s84, s84, 2
	s_addk_i32 s64, 0x100
	s_addk_i32 s65, 0x100
	s_cmp_gt_u32 s84, 29
	s_cbranch_scc0 .LBB0_114
	s_and_b64 vcc, exec, s[56:57]
	s_cbranch_vccz .LBB0_127
	s_barrier
	s_cmp_gt_i32 s61, 23
	s_mov_b64 s[46:47], -1
	s_cbranch_scc1 .LBB0_128

.LBB0_563:
	v_add_u32_e32 v3, 0x10000, v209
	ds_read_b128 v[140:143], v3
	ds_read_b128 v[144:147], v3 offset:1024
	ds_read_b128 v[148:151], v3 offset:2048
	ds_read_b128 v[152:155], v3 offset:3072
	v_add_u32_e32 v3, 0x14000, v209
	ds_read_b128 v[156:159], v3
	ds_read_b128 v[160:163], v3 offset:1024
	ds_read_b128 v[164:167], v3 offset:2048
	ds_read_b128 v[168:171], v3 offset:3072
	s_add_i32 s10, s57, 0xfff80080
	s_cmp_eq_u32 s59, 12
	s_cselect_b32 s62, s2, s10
	s_cselect_b32 s61, s3, s58
	s_add_i32 s60, s62, 0x80
	s_mov_b32 m0, s44
	ds_read_b128 v[172:175], v210
	ds_read_b128 v[176:179], v210 offset:1024
	ds_read_b128 v[180:183], v210 offset:2048
	ds_read_b128 v[184:187], v210 offset:3072
	ds_read_b128 v[188:191], v210 offset:4096
	ds_read_b128 v[192:195], v210 offset:5120
	ds_read_b128 v[196:199], v210 offset:6144
	ds_read_b128 v[200:203], v210 offset:7168
	buffer_load_dwordx4 v1, s[4:7], s57 offen lds
	s_mov_b32 m0, s45
	s_nop 0
	buffer_load_dwordx4 v206, s[4:7], s57 offen lds
	s_waitcnt vmcnt(8)
	s_waitcnt lgkmcnt(0)
	s_barrier
	s_setprio 1
	s_waitcnt lgkmcnt(7)
	v_mfma_f32_16x16x32_bf16 v[130:133], v[140:143], v[172:175], v[130:133]
	v_mfma_f32_16x16x32_bf16 v[126:129], v[148:151], v[172:175], v[126:129]
	s_waitcnt lgkmcnt(5)
	v_mfma_f32_16x16x32_bf16 v[118:121], v[148:151], v[180:183], v[118:121]
	v_mfma_f32_16x16x32_bf16 v[122:125], v[140:143], v[180:183], v[122:125]
	s_waitcnt lgkmcnt(3)
	v_mfma_f32_16x16x32_bf16 v[114:117], v[140:143], v[188:191], v[114:117]
	v_mfma_f32_16x16x32_bf16 v[110:113], v[148:151], v[188:191], v[110:113]
	s_waitcnt lgkmcnt(1)
	v_mfma_f32_16x16x32_bf16 v[102:105], v[148:151], v[196:199], v[102:105]
	v_mfma_f32_16x16x32_bf16 v[106:109], v[140:143], v[196:199], v[106:109]
	v_mfma_f32_16x16x32_bf16 v[130:133], v[144:147], v[176:179], v[130:133]
	v_mfma_f32_16x16x32_bf16 v[126:129], v[152:155], v[176:179], v[126:129]
	v_mfma_f32_16x16x32_bf16 v[118:121], v[152:155], v[184:187], v[118:121]
	v_mfma_f32_16x16x32_bf16 v[122:125], v[144:147], v[184:187], v[122:125]
	v_mfma_f32_16x16x32_bf16 v[114:117], v[144:147], v[192:195], v[114:117]
	v_mfma_f32_16x16x32_bf16 v[110:113], v[152:155], v[192:195], v[110:113]
	s_waitcnt lgkmcnt(0)
	v_mfma_f32_16x16x32_bf16 v[102:105], v[152:155], v[200:203], v[102:105]
	v_mfma_f32_16x16x32_bf16 v[106:109], v[144:147], v[200:203], v[106:109]
	s_setprio 0
	s_setprio 1
	v_mfma_f32_16x16x32_bf16 v[98:101], v[156:159], v[172:175], v[98:101]
	v_mfma_f32_16x16x32_bf16 v[94:97], v[164:167], v[172:175], v[94:97]
	v_mfma_f32_16x16x32_bf16 v[86:89], v[164:167], v[180:183], v[86:89]
	v_mfma_f32_16x16x32_bf16 v[90:93], v[156:159], v[180:183], v[90:93]
	v_mfma_f32_16x16x32_bf16 v[82:85], v[156:159], v[188:191], v[82:85]
	v_mfma_f32_16x16x32_bf16 v[78:81], v[164:167], v[188:191], v[78:81]
	v_mfma_f32_16x16x32_bf16 v[70:73], v[164:167], v[196:199], v[70:73]
	v_mfma_f32_16x16x32_bf16 v[74:77], v[156:159], v[196:199], v[74:77]
	v_mfma_f32_16x16x32_bf16 v[98:101], v[160:163], v[176:179], v[98:101]
	v_mfma_f32_16x16x32_bf16 v[94:97], v[168:171], v[176:179], v[94:97]
	v_mfma_f32_16x16x32_bf16 v[86:89], v[168:171], v[184:187], v[86:89]
	v_mfma_f32_16x16x32_bf16 v[90:93], v[160:163], v[184:187], v[90:93]
	v_mfma_f32_16x16x32_bf16 v[82:85], v[160:163], v[192:195], v[82:85]
	v_mfma_f32_16x16x32_bf16 v[78:81], v[168:171], v[192:195], v[78:81]
	v_mfma_f32_16x16x32_bf16 v[70:73], v[168:171], v[200:203], v[70:73]
	v_mfma_f32_16x16x32_bf16 v[74:77], v[160:163], v[200:203], v[74:77]
	s_setprio 0
	s_barrier
	s_mov_b32 m0, s28
	s_mov_b32 s10, s6
	s_mov_b32 s11, s7
	ds_read_b128 v[172:175], v210 offset:16384
	ds_read_b128 v[176:179], v210 offset:17408
	ds_read_b128 v[180:183], v210 offset:18432
	ds_read_b128 v[184:187], v210 offset:19456
	ds_read_b128 v[188:191], v210 offset:20480
	ds_read_b128 v[192:195], v210 offset:21504
	ds_read_b128 v[196:199], v210 offset:22528
	ds_read_b128 v[200:203], v210 offset:23552
	buffer_load_dwordx4 v135, s[8:11], s61 offen lds
	s_mov_b32 m0, s29
	s_add_i32 s63, s61, 0x80000
	buffer_load_dwordx4 v207, s[8:11], s61 offen lds
	s_mov_b32 m0, s30
	s_nop 0
	buffer_load_dwordx4 v135, s[8:11], s63 offen lds
	s_mov_b32 m0, s31
	s_nop 0
	buffer_load_dwordx4 v207, s[8:11], s63 offen lds
	s_mov_b32 m0, s27
	s_nop 0
	buffer_load_dwordx4 v1, s[4:7], s62 offen lds
	s_mov_b32 m0, s33
	s_nop 0
	buffer_load_dwordx4 v206, s[4:7], s62 offen lds
	s_waitcnt vmcnt(8)
	s_waitcnt lgkmcnt(0)
	s_barrier
	s_setprio 1
	s_waitcnt lgkmcnt(7)
	v_mfma_f32_16x16x32_bf16 v[66:69], v[140:143], v[172:175], v[66:69]
	v_mfma_f32_16x16x32_bf16 v[62:65], v[148:151], v[172:175], v[62:65]
	s_waitcnt lgkmcnt(5)
	v_mfma_f32_16x16x32_bf16 v[54:57], v[148:151], v[180:183], v[54:57]
	v_mfma_f32_16x16x32_bf16 v[58:61], v[140:143], v[180:183], v[58:61]
	s_waitcnt lgkmcnt(3)
	v_mfma_f32_16x16x32_bf16 v[50:53], v[140:143], v[188:191], v[50:53]
	v_mfma_f32_16x16x32_bf16 v[46:49], v[148:151], v[188:191], v[46:49]
	s_waitcnt lgkmcnt(1)
	v_mfma_f32_16x16x32_bf16 v[38:41], v[148:151], v[196:199], v[38:41]
	v_mfma_f32_16x16x32_bf16 v[42:45], v[140:143], v[196:199], v[42:45]
	v_mfma_f32_16x16x32_bf16 v[66:69], v[144:147], v[176:179], v[66:69]
	v_mfma_f32_16x16x32_bf16 v[62:65], v[152:155], v[176:179], v[62:65]
	v_mfma_f32_16x16x32_bf16 v[54:57], v[152:155], v[184:187], v[54:57]
	v_mfma_f32_16x16x32_bf16 v[58:61], v[144:147], v[184:187], v[58:61]
	v_mfma_f32_16x16x32_bf16 v[50:53], v[144:147], v[192:195], v[50:53]
	v_mfma_f32_16x16x32_bf16 v[46:49], v[152:155], v[192:195], v[46:49]
	s_waitcnt lgkmcnt(0)
	v_mfma_f32_16x16x32_bf16 v[38:41], v[152:155], v[200:203], v[38:41]
	v_mfma_f32_16x16x32_bf16 v[42:45], v[144:147], v[200:203], v[42:45]
	s_setprio 0
	s_setprio 1
	v_mfma_f32_16x16x32_bf16 v[34:37], v[156:159], v[172:175], v[34:37]
	v_mfma_f32_16x16x32_bf16 v[30:33], v[164:167], v[172:175], v[30:33]
	v_mfma_f32_16x16x32_bf16 v[22:25], v[164:167], v[180:183], v[22:25]
	v_mfma_f32_16x16x32_bf16 v[26:29], v[156:159], v[180:183], v[26:29]
	v_mfma_f32_16x16x32_bf16 v[18:21], v[156:159], v[188:191], v[18:21]
	v_mfma_f32_16x16x32_bf16 v[14:17], v[164:167], v[188:191], v[14:17]
	v_mfma_f32_16x16x32_bf16 v[4:7], v[164:167], v[196:199], v[6:9]
	v_mfma_f32_16x16x32_bf16 v[10:13], v[156:159], v[196:199], v[10:13]
	v_mfma_f32_16x16x32_bf16 v[34:37], v[160:163], v[176:179], v[34:37]
	v_mfma_f32_16x16x32_bf16 v[30:33], v[168:171], v[176:179], v[30:33]
	v_mfma_f32_16x16x32_bf16 v[22:25], v[168:171], v[184:187], v[22:25]
	v_mfma_f32_16x16x32_bf16 v[26:29], v[160:163], v[184:187], v[26:29]
	v_mfma_f32_16x16x32_bf16 v[18:21], v[160:163], v[192:195], v[18:21]
	v_mfma_f32_16x16x32_bf16 v[14:17], v[168:171], v[192:195], v[14:17]
	v_mfma_f32_16x16x32_bf16 v[4:7], v[168:171], v[200:203], v[4:7]
	v_mfma_f32_16x16x32_bf16 v[10:13], v[160:163], v[200:203], v[10:13]
	s_setprio 0
	s_barrier
	v_add_u32_e32 v3, 0x18000, v209
	ds_read_b128 v[140:143], v3
	ds_read_b128 v[144:147], v3 offset:1024
	ds_read_b128 v[148:151], v3 offset:2048
	ds_read_b128 v[152:155], v3 offset:3072
	v_add_u32_e32 v3, 0x1c000, v209
	ds_read_b128 v[156:159], v3
	ds_read_b128 v[160:163], v3 offset:1024
	ds_read_b128 v[164:167], v3 offset:2048
	ds_read_b128 v[168:171], v3 offset:3072
	s_add_i32 s62, s62, 0x80000
	s_mov_b32 m0, s34
	ds_read_b128 v[172:175], v210 offset:32768
	ds_read_b128 v[176:179], v210 offset:33792
	ds_read_b128 v[180:183], v210 offset:34816
	ds_read_b128 v[184:187], v210 offset:35840
	ds_read_b128 v[188:191], v210 offset:36864
	ds_read_b128 v[192:195], v210 offset:37888
	ds_read_b128 v[196:199], v210 offset:38912
	ds_read_b128 v[200:203], v210 offset:39936
	buffer_load_dwordx4 v1, s[4:7], s62 offen lds
	s_mov_b32 m0, s35
	s_nop 0
	buffer_load_dwordx4 v206, s[4:7], s62 offen lds
	s_waitcnt vmcnt(8)
	s_waitcnt lgkmcnt(0)
	s_barrier
	s_setprio 1
	s_waitcnt lgkmcnt(7)
	v_mfma_f32_16x16x32_bf16 v[130:133], v[140:143], v[172:175], v[130:133]
	v_mfma_f32_16x16x32_bf16 v[126:129], v[148:151], v[172:175], v[126:129]
	s_waitcnt lgkmcnt(5)
	v_mfma_f32_16x16x32_bf16 v[118:121], v[148:151], v[180:183], v[118:121]
	v_mfma_f32_16x16x32_bf16 v[122:125], v[140:143], v[180:183], v[122:125]
	s_waitcnt lgkmcnt(3)
	v_mfma_f32_16x16x32_bf16 v[114:117], v[140:143], v[188:191], v[114:117]
	v_mfma_f32_16x16x32_bf16 v[110:113], v[148:151], v[188:191], v[110:113]
	s_waitcnt lgkmcnt(1)
	v_mfma_f32_16x16x32_bf16 v[102:105], v[148:151], v[196:199], v[102:105]
	v_mfma_f32_16x16x32_bf16 v[106:109], v[140:143], v[196:199], v[106:109]
	v_mfma_f32_16x16x32_bf16 v[130:133], v[144:147], v[176:179], v[130:133]
	v_mfma_f32_16x16x32_bf16 v[126:129], v[152:155], v[176:179], v[126:129]
	v_mfma_f32_16x16x32_bf16 v[118:121], v[152:155], v[184:187], v[118:121]
	v_mfma_f32_16x16x32_bf16 v[122:125], v[144:147], v[184:187], v[122:125]
	v_mfma_f32_16x16x32_bf16 v[114:117], v[144:147], v[192:195], v[114:117]
	v_mfma_f32_16x16x32_bf16 v[110:113], v[152:155], v[192:195], v[110:113]
	s_waitcnt lgkmcnt(0)
	v_mfma_f32_16x16x32_bf16 v[102:105], v[152:155], v[200:203], v[102:105]
	v_mfma_f32_16x16x32_bf16 v[106:109], v[144:147], v[200:203], v[106:109]
	s_setprio 0
	s_setprio 1
	v_mfma_f32_16x16x32_bf16 v[98:101], v[156:159], v[172:175], v[98:101]
	v_mfma_f32_16x16x32_bf16 v[94:97], v[164:167], v[172:175], v[94:97]
	v_mfma_f32_16x16x32_bf16 v[86:89], v[164:167], v[180:183], v[86:89]
	v_mfma_f32_16x16x32_bf16 v[90:93], v[156:159], v[180:183], v[90:93]
	v_mfma_f32_16x16x32_bf16 v[82:85], v[156:159], v[188:191], v[82:85]
	v_mfma_f32_16x16x32_bf16 v[78:81], v[164:167], v[188:191], v[78:81]
	v_mfma_f32_16x16x32_bf16 v[70:73], v[164:167], v[196:199], v[70:73]
	v_mfma_f32_16x16x32_bf16 v[74:77], v[156:159], v[196:199], v[74:77]
	v_mfma_f32_16x16x32_bf16 v[98:101], v[160:163], v[176:179], v[98:101]
	v_mfma_f32_16x16x32_bf16 v[94:97], v[168:171], v[176:179], v[94:97]
	v_mfma_f32_16x16x32_bf16 v[86:89], v[168:171], v[184:187], v[86:89]
	v_mfma_f32_16x16x32_bf16 v[90:93], v[160:163], v[184:187], v[90:93]
	v_mfma_f32_16x16x32_bf16 v[82:85], v[160:163], v[192:195], v[82:85]
	v_mfma_f32_16x16x32_bf16 v[78:81], v[168:171], v[192:195], v[78:81]
	v_mfma_f32_16x16x32_bf16 v[70:73], v[168:171], v[200:203], v[70:73]
	v_mfma_f32_16x16x32_bf16 v[74:77], v[160:163], v[200:203], v[74:77]
	s_setprio 0
	s_barrier
	s_mov_b32 m0, s38
	s_add_i32 s62, s61, 0x80
	ds_read_b128 v[172:175], v210 offset:49152
	ds_read_b128 v[176:179], v210 offset:50176
	ds_read_b128 v[180:183], v210 offset:51200
	ds_read_b128 v[184:187], v210 offset:52224
	ds_read_b128 v[188:191], v210 offset:53248
	ds_read_b128 v[192:195], v210 offset:54272
	ds_read_b128 v[196:199], v210 offset:55296
	ds_read_b128 v[200:203], v210 offset:56320
	buffer_load_dwordx4 v135, s[8:11], s62 offen lds
	s_mov_b32 m0, s39
	s_add_i32 s61, s61, 0x80080
	buffer_load_dwordx4 v207, s[8:11], s62 offen lds
	s_mov_b32 m0, s42
	s_nop 0
	buffer_load_dwordx4 v135, s[8:11], s61 offen lds
	s_mov_b32 m0, s43
	s_nop 0
	buffer_load_dwordx4 v207, s[8:11], s61 offen lds
	s_mov_b32 m0, s40
	s_nop 0
	buffer_load_dwordx4 v1, s[4:7], s60 offen lds
	s_mov_b32 m0, s41
	s_nop 0
	buffer_load_dwordx4 v206, s[4:7], s60 offen lds
	s_waitcnt vmcnt(8)
	s_waitcnt lgkmcnt(0)
	s_barrier
	s_setprio 1
	s_waitcnt lgkmcnt(7)
	v_mfma_f32_16x16x32_bf16 v[66:69], v[140:143], v[172:175], v[66:69]
	v_mfma_f32_16x16x32_bf16 v[62:65], v[148:151], v[172:175], v[62:65]
	s_waitcnt lgkmcnt(5)
	v_mfma_f32_16x16x32_bf16 v[54:57], v[148:151], v[180:183], v[54:57]
	v_mfma_f32_16x16x32_bf16 v[58:61], v[140:143], v[180:183], v[58:61]
	s_waitcnt lgkmcnt(3)
	v_mfma_f32_16x16x32_bf16 v[50:53], v[140:143], v[188:191], v[50:53]
	v_mfma_f32_16x16x32_bf16 v[46:49], v[148:151], v[188:191], v[46:49]
	s_waitcnt lgkmcnt(1)
	v_mfma_f32_16x16x32_bf16 v[38:41], v[148:151], v[196:199], v[38:41]
	v_mfma_f32_16x16x32_bf16 v[42:45], v[140:143], v[196:199], v[42:45]
	v_mfma_f32_16x16x32_bf16 v[66:69], v[144:147], v[176:179], v[66:69]
	v_mfma_f32_16x16x32_bf16 v[62:65], v[152:155], v[176:179], v[62:65]
	v_mfma_f32_16x16x32_bf16 v[54:57], v[152:155], v[184:187], v[54:57]
	v_mfma_f32_16x16x32_bf16 v[58:61], v[144:147], v[184:187], v[58:61]
	v_mfma_f32_16x16x32_bf16 v[50:53], v[144:147], v[192:195], v[50:53]
	v_mfma_f32_16x16x32_bf16 v[46:49], v[152:155], v[192:195], v[46:49]
	s_waitcnt lgkmcnt(0)
	v_mfma_f32_16x16x32_bf16 v[38:41], v[152:155], v[200:203], v[38:41]
	v_mfma_f32_16x16x32_bf16 v[42:45], v[144:147], v[200:203], v[42:45]
	s_setprio 0
	s_setprio 1
	v_mfma_f32_16x16x32_bf16 v[34:37], v[156:159], v[172:175], v[34:37]
	v_mfma_f32_16x16x32_bf16 v[30:33], v[164:167], v[172:175], v[30:33]
	v_mfma_f32_16x16x32_bf16 v[22:25], v[164:167], v[180:183], v[22:25]
	v_mfma_f32_16x16x32_bf16 v[26:29], v[156:159], v[180:183], v[26:29]
	v_mfma_f32_16x16x32_bf16 v[18:21], v[156:159], v[188:191], v[18:21]
	v_mfma_f32_16x16x32_bf16 v[14:17], v[164:167], v[188:191], v[14:17]
	v_mfma_f32_16x16x32_bf16 v[4:7], v[164:167], v[196:199], v[4:7]
	v_mfma_f32_16x16x32_bf16 v[8:11], v[156:159], v[196:199], v[10:13]
	v_mfma_f32_16x16x32_bf16 v[34:37], v[160:163], v[176:179], v[34:37]
	v_mfma_f32_16x16x32_bf16 v[30:33], v[168:171], v[176:179], v[30:33]
	v_mfma_f32_16x16x32_bf16 v[22:25], v[168:171], v[184:187], v[22:25]
	v_mfma_f32_16x16x32_bf16 v[26:29], v[160:163], v[184:187], v[26:29]
	v_mfma_f32_16x16x32_bf16 v[18:21], v[160:163], v[192:195], v[18:21]
	v_mfma_f32_16x16x32_bf16 v[14:17], v[168:171], v[192:195], v[14:17]
	v_mfma_f32_16x16x32_bf16 v[6:9], v[168:171], v[200:203], v[4:7]
	v_mfma_f32_16x16x32_bf16 v[10:13], v[160:163], v[200:203], v[8:11]
	s_setprio 0
	s_barrier
	s_add_i32 s59, s59, 2
	s_addk_i32 s57, 0x100
	s_addk_i32 s58, 0x100
	s_cmp_gt_u32 s59, 13
	s_cbranch_scc0 .LBB0_563
	s_and_b64 vcc, exec, s[20:21]
	s_cbranch_vccz .LBB0_566
	s_barrier

.LBB0_686:
	v_add_u32_e32 v152, 0x10000, v138
	v_add_u32_e32 v168, 0x14000, v138
	ds_read_b128 v[140:143], v152
	ds_read_b128 v[144:147], v152 offset:1024
	ds_read_b128 v[148:151], v152 offset:2048
	ds_read_b128 v[152:155], v152 offset:3072
	ds_read_b128 v[156:159], v168
	ds_read_b128 v[160:163], v168 offset:1024
	ds_read_b128 v[164:167], v168 offset:2048
	ds_read_b128 v[168:171], v168 offset:3072
	s_add_i32 s10, s33, s52
	s_add_i32 s53, s27, s52
	s_add_i32 s11, s10, 0x1000
	s_addk_i32 s53, 0x1000
	s_cmp_eq_u32 s52, 0
	s_cselect_b32 s55, s49, s11
	s_cselect_b32 s54, s50, s53
	s_or_b32 s53, s55, 0x80
	s_add_i32 s10, s10, 0x80f80
	s_mov_b32 m0, s43
	ds_read_b128 v[172:175], v139
	ds_read_b128 v[176:179], v139 offset:1024
	ds_read_b128 v[180:183], v139 offset:2048
	ds_read_b128 v[184:187], v139 offset:3072
	ds_read_b128 v[188:191], v139 offset:4096
	ds_read_b128 v[192:195], v139 offset:5120
	ds_read_b128 v[196:199], v139 offset:6144
	ds_read_b128 v[200:203], v139 offset:7168
	buffer_load_dwordx4 v134, s[4:7], s10 offen lds
	s_mov_b32 m0, s44
	s_nop 0
	buffer_load_dwordx4 v136, s[4:7], s10 offen lds
	s_waitcnt vmcnt(8)
	s_waitcnt lgkmcnt(0)
	s_barrier
	s_setprio 1
	s_waitcnt lgkmcnt(7)
	v_mfma_f32_16x16x32_bf16 v[126:129], v[140:143], v[172:175], v[126:129]
	v_mfma_f32_16x16x32_bf16 v[122:125], v[148:151], v[172:175], v[122:125]
	s_waitcnt lgkmcnt(5)
	v_mfma_f32_16x16x32_bf16 v[106:109], v[148:151], v[180:183], v[106:109]
	v_mfma_f32_16x16x32_bf16 v[110:113], v[140:143], v[180:183], v[110:113]
	s_waitcnt lgkmcnt(3)
	v_mfma_f32_16x16x32_bf16 v[98:101], v[140:143], v[188:191], v[98:101]
	v_mfma_f32_16x16x32_bf16 v[90:93], v[148:151], v[188:191], v[90:93]
	s_waitcnt lgkmcnt(1)
	v_mfma_f32_16x16x32_bf16 v[74:77], v[148:151], v[196:199], v[74:77]
	v_mfma_f32_16x16x32_bf16 v[82:85], v[140:143], v[196:199], v[82:85]
	v_mfma_f32_16x16x32_bf16 v[126:129], v[144:147], v[176:179], v[126:129]
	v_mfma_f32_16x16x32_bf16 v[122:125], v[152:155], v[176:179], v[122:125]
	v_mfma_f32_16x16x32_bf16 v[106:109], v[152:155], v[184:187], v[106:109]
	v_mfma_f32_16x16x32_bf16 v[110:113], v[144:147], v[184:187], v[110:113]
	v_mfma_f32_16x16x32_bf16 v[98:101], v[144:147], v[192:195], v[98:101]
	v_mfma_f32_16x16x32_bf16 v[90:93], v[152:155], v[192:195], v[90:93]
	s_waitcnt lgkmcnt(0)
	v_mfma_f32_16x16x32_bf16 v[74:77], v[152:155], v[200:203], v[74:77]
	v_mfma_f32_16x16x32_bf16 v[82:85], v[144:147], v[200:203], v[82:85]
	s_setprio 0
	s_setprio 1
	v_mfma_f32_16x16x32_bf16 v[118:121], v[156:159], v[172:175], v[118:121]
	v_mfma_f32_16x16x32_bf16 v[114:117], v[164:167], v[172:175], v[114:117]
	v_mfma_f32_16x16x32_bf16 v[94:97], v[164:167], v[180:183], v[94:97]
	v_mfma_f32_16x16x32_bf16 v[102:105], v[156:159], v[180:183], v[102:105]
	v_mfma_f32_16x16x32_bf16 v[86:89], v[156:159], v[188:191], v[86:89]
	v_mfma_f32_16x16x32_bf16 v[78:81], v[164:167], v[188:191], v[78:81]
	v_mfma_f32_16x16x32_bf16 v[66:69], v[164:167], v[196:199], v[66:69]
	v_mfma_f32_16x16x32_bf16 v[70:73], v[156:159], v[196:199], v[70:73]
	v_mfma_f32_16x16x32_bf16 v[118:121], v[160:163], v[176:179], v[118:121]
	v_mfma_f32_16x16x32_bf16 v[114:117], v[168:171], v[176:179], v[114:117]
	v_mfma_f32_16x16x32_bf16 v[94:97], v[168:171], v[184:187], v[94:97]
	v_mfma_f32_16x16x32_bf16 v[102:105], v[160:163], v[184:187], v[102:105]
	v_mfma_f32_16x16x32_bf16 v[86:89], v[160:163], v[192:195], v[86:89]
	v_mfma_f32_16x16x32_bf16 v[78:81], v[168:171], v[192:195], v[78:81]
	v_mfma_f32_16x16x32_bf16 v[66:69], v[168:171], v[200:203], v[66:69]
	v_mfma_f32_16x16x32_bf16 v[70:73], v[160:163], v[200:203], v[70:73]
	s_setprio 0
	s_barrier
	s_mov_b32 m0, s26
	s_mov_b32 s10, s6
	s_mov_b32 s11, s7
	ds_read_b128 v[172:175], v139 offset:16384
	ds_read_b128 v[176:179], v139 offset:17408
	ds_read_b128 v[180:183], v139 offset:18432
	ds_read_b128 v[184:187], v139 offset:19456
	ds_read_b128 v[188:191], v139 offset:20480
	ds_read_b128 v[192:195], v139 offset:21504
	ds_read_b128 v[196:199], v139 offset:22528
	ds_read_b128 v[200:203], v139 offset:23552
	buffer_load_dwordx4 v135, s[8:11], s54 offen lds
	s_mov_b32 m0, s28
	s_add_i32 s56, s54, 0x80000
	buffer_load_dwordx4 v137, s[8:11], s54 offen lds
	s_mov_b32 m0, s29
	s_nop 0
	buffer_load_dwordx4 v135, s[8:11], s56 offen lds
	s_mov_b32 m0, s30
	s_nop 0
	buffer_load_dwordx4 v137, s[8:11], s56 offen lds
	s_mov_b32 m0, s25
	s_nop 0
	buffer_load_dwordx4 v134, s[4:7], s55 offen lds
	s_mov_b32 m0, s31
	s_nop 0
	buffer_load_dwordx4 v136, s[4:7], s55 offen lds
	s_waitcnt vmcnt(8)
	s_waitcnt lgkmcnt(0)
	s_barrier
	s_setprio 1
	s_waitcnt lgkmcnt(7)
	v_mfma_f32_16x16x32_bf16 v[62:65], v[140:143], v[172:175], v[62:65]
	v_mfma_f32_16x16x32_bf16 v[58:61], v[148:151], v[172:175], v[58:61]
	s_waitcnt lgkmcnt(5)
	v_mfma_f32_16x16x32_bf16 v[42:45], v[148:151], v[180:183], v[42:45]
	v_mfma_f32_16x16x32_bf16 v[46:49], v[140:143], v[180:183], v[46:49]
	s_waitcnt lgkmcnt(3)
	v_mfma_f32_16x16x32_bf16 v[30:33], v[140:143], v[188:191], v[30:33]
	v_mfma_f32_16x16x32_bf16 v[26:29], v[148:151], v[188:191], v[26:29]
	s_waitcnt lgkmcnt(1)
	v_mfma_f32_16x16x32_bf16 v[10:13], v[148:151], v[196:199], v[10:13]
	v_mfma_f32_16x16x32_bf16 v[14:17], v[140:143], v[196:199], v[14:17]
	v_mfma_f32_16x16x32_bf16 v[62:65], v[144:147], v[176:179], v[62:65]
	v_mfma_f32_16x16x32_bf16 v[58:61], v[152:155], v[176:179], v[58:61]
	v_mfma_f32_16x16x32_bf16 v[42:45], v[152:155], v[184:187], v[42:45]
	v_mfma_f32_16x16x32_bf16 v[46:49], v[144:147], v[184:187], v[46:49]
	v_mfma_f32_16x16x32_bf16 v[30:33], v[144:147], v[192:195], v[30:33]
	v_mfma_f32_16x16x32_bf16 v[26:29], v[152:155], v[192:195], v[26:29]
	s_waitcnt lgkmcnt(0)
	v_mfma_f32_16x16x32_bf16 v[10:13], v[152:155], v[200:203], v[10:13]
	v_mfma_f32_16x16x32_bf16 v[14:17], v[144:147], v[200:203], v[14:17]
	s_setprio 0
	s_setprio 1
	v_mfma_f32_16x16x32_bf16 v[54:57], v[156:159], v[172:175], v[54:57]
	v_mfma_f32_16x16x32_bf16 v[50:53], v[164:167], v[172:175], v[50:53]
	v_mfma_f32_16x16x32_bf16 v[34:37], v[164:167], v[180:183], v[34:37]
	v_mfma_f32_16x16x32_bf16 v[38:41], v[156:159], v[180:183], v[38:41]
	v_mfma_f32_16x16x32_bf16 v[22:25], v[156:159], v[188:191], v[22:25]
	v_mfma_f32_16x16x32_bf16 v[18:21], v[164:167], v[188:191], v[18:21]
	v_mfma_f32_16x16x32_bf16 v[2:5], v[164:167], v[196:199], v[2:5]
	v_mfma_f32_16x16x32_bf16 v[6:9], v[156:159], v[196:199], v[6:9]
	v_mfma_f32_16x16x32_bf16 v[54:57], v[160:163], v[176:179], v[54:57]
	v_mfma_f32_16x16x32_bf16 v[50:53], v[168:171], v[176:179], v[50:53]
	v_mfma_f32_16x16x32_bf16 v[34:37], v[168:171], v[184:187], v[34:37]
	v_mfma_f32_16x16x32_bf16 v[38:41], v[160:163], v[184:187], v[38:41]
	v_mfma_f32_16x16x32_bf16 v[22:25], v[160:163], v[192:195], v[22:25]
	v_mfma_f32_16x16x32_bf16 v[18:21], v[168:171], v[192:195], v[18:21]
	v_mfma_f32_16x16x32_bf16 v[2:5], v[168:171], v[200:203], v[2:5]
	v_mfma_f32_16x16x32_bf16 v[6:9], v[160:163], v[200:203], v[6:9]
	s_setprio 0
	s_barrier
	v_add_u32_e32 v152, 0x18000, v138
	v_add_u32_e32 v168, 0x1c000, v138
	ds_read_b128 v[140:143], v152
	ds_read_b128 v[144:147], v152 offset:1024
	ds_read_b128 v[148:151], v152 offset:2048
	ds_read_b128 v[152:155], v152 offset:3072
	ds_read_b128 v[156:159], v168
	ds_read_b128 v[160:163], v168 offset:1024
	ds_read_b128 v[164:167], v168 offset:2048
	ds_read_b128 v[168:171], v168 offset:3072
	s_add_i32 s55, s55, 0x80000
	s_mov_b32 m0, s34
	ds_read_b128 v[172:175], v139 offset:32768
	ds_read_b128 v[176:179], v139 offset:33792
	ds_read_b128 v[180:183], v139 offset:34816
	ds_read_b128 v[184:187], v139 offset:35840
	ds_read_b128 v[188:191], v139 offset:36864
	ds_read_b128 v[192:195], v139 offset:37888
	ds_read_b128 v[196:199], v139 offset:38912
	ds_read_b128 v[200:203], v139 offset:39936
	buffer_load_dwordx4 v134, s[4:7], s55 offen lds
	s_mov_b32 m0, s35
	s_nop 0
	buffer_load_dwordx4 v136, s[4:7], s55 offen lds
	s_waitcnt vmcnt(8)
	s_waitcnt lgkmcnt(0)
	s_barrier
	s_setprio 1
	s_waitcnt lgkmcnt(7)
	v_mfma_f32_16x16x32_bf16 v[126:129], v[140:143], v[172:175], v[126:129]
	v_mfma_f32_16x16x32_bf16 v[122:125], v[148:151], v[172:175], v[122:125]
	s_waitcnt lgkmcnt(5)
	v_mfma_f32_16x16x32_bf16 v[106:109], v[148:151], v[180:183], v[106:109]
	v_mfma_f32_16x16x32_bf16 v[110:113], v[140:143], v[180:183], v[110:113]
	s_waitcnt lgkmcnt(3)
	v_mfma_f32_16x16x32_bf16 v[98:101], v[140:143], v[188:191], v[98:101]
	v_mfma_f32_16x16x32_bf16 v[90:93], v[148:151], v[188:191], v[90:93]
	s_waitcnt lgkmcnt(1)
	v_mfma_f32_16x16x32_bf16 v[74:77], v[148:151], v[196:199], v[74:77]
	v_mfma_f32_16x16x32_bf16 v[82:85], v[140:143], v[196:199], v[82:85]
	v_mfma_f32_16x16x32_bf16 v[126:129], v[144:147], v[176:179], v[126:129]
	v_mfma_f32_16x16x32_bf16 v[122:125], v[152:155], v[176:179], v[122:125]
	v_mfma_f32_16x16x32_bf16 v[106:109], v[152:155], v[184:187], v[106:109]
	v_mfma_f32_16x16x32_bf16 v[110:113], v[144:147], v[184:187], v[110:113]
	v_mfma_f32_16x16x32_bf16 v[98:101], v[144:147], v[192:195], v[98:101]
	v_mfma_f32_16x16x32_bf16 v[90:93], v[152:155], v[192:195], v[90:93]
	s_waitcnt lgkmcnt(0)
	v_mfma_f32_16x16x32_bf16 v[74:77], v[152:155], v[200:203], v[74:77]
	v_mfma_f32_16x16x32_bf16 v[82:85], v[144:147], v[200:203], v[82:85]
	s_setprio 0
	s_setprio 1
	v_mfma_f32_16x16x32_bf16 v[118:121], v[156:159], v[172:175], v[118:121]
	v_mfma_f32_16x16x32_bf16 v[114:117], v[164:167], v[172:175], v[114:117]
	v_mfma_f32_16x16x32_bf16 v[94:97], v[164:167], v[180:183], v[94:97]
	v_mfma_f32_16x16x32_bf16 v[102:105], v[156:159], v[180:183], v[102:105]
	v_mfma_f32_16x16x32_bf16 v[86:89], v[156:159], v[188:191], v[86:89]
	v_mfma_f32_16x16x32_bf16 v[78:81], v[164:167], v[188:191], v[78:81]
	v_mfma_f32_16x16x32_bf16 v[66:69], v[164:167], v[196:199], v[66:69]
	v_mfma_f32_16x16x32_bf16 v[70:73], v[156:159], v[196:199], v[70:73]
	v_mfma_f32_16x16x32_bf16 v[118:121], v[160:163], v[176:179], v[118:121]
	v_mfma_f32_16x16x32_bf16 v[114:117], v[168:171], v[176:179], v[114:117]
	v_mfma_f32_16x16x32_bf16 v[94:97], v[168:171], v[184:187], v[94:97]
	v_mfma_f32_16x16x32_bf16 v[102:105], v[160:163], v[184:187], v[102:105]
	v_mfma_f32_16x16x32_bf16 v[86:89], v[160:163], v[192:195], v[86:89]
	v_mfma_f32_16x16x32_bf16 v[78:81], v[168:171], v[192:195], v[78:81]
	v_mfma_f32_16x16x32_bf16 v[66:69], v[168:171], v[200:203], v[66:69]
	v_mfma_f32_16x16x32_bf16 v[70:73], v[160:163], v[200:203], v[70:73]
	s_setprio 0
	s_barrier
	s_mov_b32 m0, s36
	s_or_b32 s55, s54, 0x80
	ds_read_b128 v[172:175], v139 offset:49152
	ds_read_b128 v[176:179], v139 offset:50176
	ds_read_b128 v[180:183], v139 offset:51200
	ds_read_b128 v[184:187], v139 offset:52224
	ds_read_b128 v[188:191], v139 offset:53248
	ds_read_b128 v[192:195], v139 offset:54272
	ds_read_b128 v[196:199], v139 offset:55296
	ds_read_b128 v[200:203], v139 offset:56320
	buffer_load_dwordx4 v135, s[8:11], s55 offen lds
	s_mov_b32 m0, s37
	s_add_i32 s54, s54, 0x80080
	buffer_load_dwordx4 v137, s[8:11], s55 offen lds
	s_mov_b32 m0, s41
	s_nop 0
	buffer_load_dwordx4 v135, s[8:11], s54 offen lds
	s_mov_b32 m0, s42
	s_nop 0
	buffer_load_dwordx4 v137, s[8:11], s54 offen lds
	s_mov_b32 m0, s38
	s_nop 0
	buffer_load_dwordx4 v134, s[4:7], s53 offen lds
	s_mov_b32 m0, s40
	s_nop 0
	buffer_load_dwordx4 v136, s[4:7], s53 offen lds
	s_waitcnt vmcnt(8)
	s_waitcnt lgkmcnt(0)
	s_barrier
	s_setprio 1
	s_waitcnt lgkmcnt(7)
	v_mfma_f32_16x16x32_bf16 v[62:65], v[140:143], v[172:175], v[62:65]
	v_mfma_f32_16x16x32_bf16 v[58:61], v[148:151], v[172:175], v[58:61]
	s_waitcnt lgkmcnt(5)
	v_mfma_f32_16x16x32_bf16 v[42:45], v[148:151], v[180:183], v[42:45]
	v_mfma_f32_16x16x32_bf16 v[46:49], v[140:143], v[180:183], v[46:49]
	s_waitcnt lgkmcnt(3)
	v_mfma_f32_16x16x32_bf16 v[30:33], v[140:143], v[188:191], v[30:33]
	v_mfma_f32_16x16x32_bf16 v[26:29], v[148:151], v[188:191], v[26:29]
	s_waitcnt lgkmcnt(1)
	v_mfma_f32_16x16x32_bf16 v[10:13], v[148:151], v[196:199], v[10:13]
	v_mfma_f32_16x16x32_bf16 v[14:17], v[140:143], v[196:199], v[14:17]
	v_mfma_f32_16x16x32_bf16 v[62:65], v[144:147], v[176:179], v[62:65]
	v_mfma_f32_16x16x32_bf16 v[58:61], v[152:155], v[176:179], v[58:61]
	v_mfma_f32_16x16x32_bf16 v[42:45], v[152:155], v[184:187], v[42:45]
	v_mfma_f32_16x16x32_bf16 v[46:49], v[144:147], v[184:187], v[46:49]
	v_mfma_f32_16x16x32_bf16 v[30:33], v[144:147], v[192:195], v[30:33]
	v_mfma_f32_16x16x32_bf16 v[26:29], v[152:155], v[192:195], v[26:29]
	s_waitcnt lgkmcnt(0)
	v_mfma_f32_16x16x32_bf16 v[10:13], v[152:155], v[200:203], v[10:13]
	v_mfma_f32_16x16x32_bf16 v[14:17], v[144:147], v[200:203], v[14:17]
	s_setprio 0
	s_setprio 1
	v_mfma_f32_16x16x32_bf16 v[54:57], v[156:159], v[172:175], v[54:57]
	v_mfma_f32_16x16x32_bf16 v[50:53], v[164:167], v[172:175], v[50:53]
	v_mfma_f32_16x16x32_bf16 v[34:37], v[164:167], v[180:183], v[34:37]
	v_mfma_f32_16x16x32_bf16 v[38:41], v[156:159], v[180:183], v[38:41]
	v_mfma_f32_16x16x32_bf16 v[22:25], v[156:159], v[188:191], v[22:25]
	v_mfma_f32_16x16x32_bf16 v[18:21], v[164:167], v[188:191], v[18:21]
	v_mfma_f32_16x16x32_bf16 v[2:5], v[164:167], v[196:199], v[2:5]
	v_mfma_f32_16x16x32_bf16 v[6:9], v[156:159], v[196:199], v[6:9]
	v_mfma_f32_16x16x32_bf16 v[54:57], v[160:163], v[176:179], v[54:57]
	v_mfma_f32_16x16x32_bf16 v[50:53], v[168:171], v[176:179], v[50:53]
	v_mfma_f32_16x16x32_bf16 v[34:37], v[168:171], v[184:187], v[34:37]
	v_mfma_f32_16x16x32_bf16 v[38:41], v[160:163], v[184:187], v[38:41]
	v_mfma_f32_16x16x32_bf16 v[22:25], v[160:163], v[192:195], v[22:25]
	v_mfma_f32_16x16x32_bf16 v[18:21], v[168:171], v[192:195], v[18:21]
	v_mfma_f32_16x16x32_bf16 v[2:5], v[168:171], v[200:203], v[2:5]
	v_mfma_f32_16x16x32_bf16 v[6:9], v[160:163], v[200:203], v[6:9]
	s_setprio 0
	s_barrier
	s_add_i32 s51, s51, 2
	s_addk_i32 s52, 0x100
	s_cmp_gt_u32 s51, 29
	s_cbranch_scc0 .LBB0_686
	s_andn2_b64 vcc, exec, s[2:3]
	s_cbranch_vccnz .LBB0_678
	v_mov_b32_e32 v2, 0
	s_mov_b32 s14, s46
	s_mov_b32 s15, s47
	s_mov_b32 s27, s48
	s_mov_b32 s33, s13
	s_mov_b32 s45, s12
	v_mov_b32_e32 v3, v2
	v_mov_b32_e32 v4, v2
	v_mov_b32_e32 v5, v2
	v_mov_b32_e32 v6, v2
	v_mov_b32_e32 v7, v2
	v_mov_b32_e32 v8, v2
	v_mov_b32_e32 v9, v2
	v_mov_b32_e32 v18, v2
	v_mov_b32_e32 v19, v2
	v_mov_b32_e32 v20, v2
	v_mov_b32_e32 v21, v2
	v_mov_b32_e32 v22, v2
	v_mov_b32_e32 v23, v2
	v_mov_b32_e32 v24, v2
	v_mov_b32_e32 v25, v2
	v_mov_b32_e32 v34, v2
	v_mov_b32_e32 v35, v2
	v_mov_b32_e32 v36, v2
	v_mov_b32_e32 v37, v2
	v_mov_b32_e32 v38, v2
	v_mov_b32_e32 v39, v2
	v_mov_b32_e32 v40, v2
	v_mov_b32_e32 v41, v2
	v_mov_b32_e32 v50, v2
	v_mov_b32_e32 v51, v2
	v_mov_b32_e32 v52, v2
	v_mov_b32_e32 v53, v2
	v_mov_b32_e32 v54, v2
	v_mov_b32_e32 v55, v2
	v_mov_b32_e32 v56, v2
	v_mov_b32_e32 v57, v2
	v_mov_b32_e32 v10, v2
	v_mov_b32_e32 v11, v2
	v_mov_b32_e32 v12, v2
	v_mov_b32_e32 v13, v2
	v_mov_b32_e32 v14, v2
	v_mov_b32_e32 v15, v2
	v_mov_b32_e32 v16, v2
	v_mov_b32_e32 v17, v2
	v_mov_b32_e32 v26, v2
	v_mov_b32_e32 v27, v2
	v_mov_b32_e32 v28, v2
	v_mov_b32_e32 v29, v2
	v_mov_b32_e32 v30, v2
	v_mov_b32_e32 v31, v2
	v_mov_b32_e32 v32, v2
	v_mov_b32_e32 v33, v2
	v_mov_b32_e32 v42, v2
	v_mov_b32_e32 v43, v2
	v_mov_b32_e32 v44, v2
	v_mov_b32_e32 v45, v2
	v_mov_b32_e32 v46, v2
	v_mov_b32_e32 v47, v2
	v_mov_b32_e32 v48, v2
	v_mov_b32_e32 v49, v2
	v_mov_b32_e32 v58, v2
	v_mov_b32_e32 v59, v2
	v_mov_b32_e32 v60, v2
	v_mov_b32_e32 v61, v2
	v_mov_b32_e32 v62, v2
	v_mov_b32_e32 v63, v2
	v_mov_b32_e32 v64, v2
	v_mov_b32_e32 v65, v2
	v_mov_b32_e32 v66, v2
	v_mov_b32_e32 v67, v2
	v_mov_b32_e32 v68, v2
	v_mov_b32_e32 v69, v2
	v_mov_b32_e32 v70, v2
	v_mov_b32_e32 v71, v2
	v_mov_b32_e32 v72, v2
	v_mov_b32_e32 v73, v2
	v_mov_b32_e32 v78, v2
	v_mov_b32_e32 v79, v2
	v_mov_b32_e32 v80, v2
	v_mov_b32_e32 v81, v2
	v_mov_b32_e32 v86, v2
	v_mov_b32_e32 v87, v2
	v_mov_b32_e32 v88, v2
	v_mov_b32_e32 v89, v2
	v_mov_b32_e32 v94, v2
	v_mov_b32_e32 v95, v2
	v_mov_b32_e32 v96, v2
	v_mov_b32_e32 v97, v2
	v_mov_b32_e32 v102, v2
	v_mov_b32_e32 v103, v2
	v_mov_b32_e32 v104, v2
	v_mov_b32_e32 v105, v2
	v_mov_b32_e32 v114, v2
	v_mov_b32_e32 v115, v2
	v_mov_b32_e32 v116, v2
	v_mov_b32_e32 v117, v2
	v_mov_b32_e32 v118, v2
	v_mov_b32_e32 v119, v2
	v_mov_b32_e32 v120, v2
	v_mov_b32_e32 v121, v2
	v_mov_b32_e32 v74, v2
	v_mov_b32_e32 v75, v2
	v_mov_b32_e32 v76, v2
	v_mov_b32_e32 v77, v2
	v_mov_b32_e32 v82, v2
	v_mov_b32_e32 v83, v2
	v_mov_b32_e32 v84, v2
	v_mov_b32_e32 v85, v2
	v_mov_b32_e32 v90, v2
	v_mov_b32_e32 v91, v2
	v_mov_b32_e32 v92, v2
	v_mov_b32_e32 v93, v2
	v_mov_b32_e32 v98, v2
	v_mov_b32_e32 v99, v2
	v_mov_b32_e32 v100, v2
	v_mov_b32_e32 v101, v2
	v_mov_b32_e32 v106, v2
	v_mov_b32_e32 v107, v2
	v_mov_b32_e32 v108, v2
	v_mov_b32_e32 v109, v2
	v_mov_b32_e32 v110, v2
	v_mov_b32_e32 v111, v2
	v_mov_b32_e32 v112, v2
	v_mov_b32_e32 v113, v2
	v_mov_b32_e32 v122, v2
	v_mov_b32_e32 v123, v2
	v_mov_b32_e32 v124, v2
	v_mov_b32_e32 v125, v2
	v_mov_b32_e32 v126, v2
	v_mov_b32_e32 v127, v2
	v_mov_b32_e32 v128, v2
	v_mov_b32_e32 v129, v2
	s_branch .LBB0_678

.LBB0_907:
	v_add_u32_e32 v166, 0x10000, v179
	ds_read_b128 v[162:165], v166
	ds_read_b128 v[182:185], v166 offset:1024
	ds_read_b128 v[186:189], v166 offset:2048
	ds_read_b128 v[190:193], v166 offset:3072
	v_add_u32_e32 v166, 0x14000, v179
	ds_read_b128 v[194:197], v166
	ds_read_b128 v[198:201], v166 offset:1024
	ds_read_b128 v[202:205], v166 offset:2048
	ds_read_b128 v[206:209], v166 offset:3072
	s_add_i32 s10, s45, s64
	s_add_i32 s26, s40, s64
	s_add_i32 s11, s10, 0x1000
	s_addk_i32 s26, 0x1000
	s_cmp_eq_u32 s64, 0
	s_cselect_b32 s29, s62, s11
	s_cselect_b32 s27, s63, s26
	s_add_i32 s26, s29, 0x80
	s_add_i32 s28, s27, 0x80
	s_add_i32 s10, s10, 0x80f80
	s_mov_b32 m0, s55
	ds_read_b128 v[210:213], v180
	ds_read_b128 v[214:217], v180 offset:1024
	ds_read_b128 v[218:221], v180 offset:2048
	ds_read_b128 v[222:225], v180 offset:3072
	ds_read_b128 v[226:229], v180 offset:4096
	ds_read_b128 v[230:233], v180 offset:5120
	ds_read_b128 v[234:237], v180 offset:6144
	ds_read_b128 v[238:241], v180 offset:7168
	buffer_load_dwordx4 v1, s[4:7], s10 offen lds
	s_mov_b32 m0, s56
	s_nop 0
	buffer_load_dwordx4 v175, s[4:7], s10 offen lds
	s_waitcnt vmcnt(8)
	s_waitcnt lgkmcnt(0)
	s_barrier
	s_setprio 1
	s_waitcnt lgkmcnt(7)
	v_mfma_f32_16x16x32_bf16 v[126:129], v[162:165], v[210:213], v[126:129]
	v_mfma_f32_16x16x32_bf16 v[122:125], v[186:189], v[210:213], v[122:125]
	s_waitcnt lgkmcnt(5)
	v_mfma_f32_16x16x32_bf16 v[114:117], v[186:189], v[218:221], v[114:117]
	v_mfma_f32_16x16x32_bf16 v[118:121], v[162:165], v[218:221], v[118:121]
	s_waitcnt lgkmcnt(3)
	v_mfma_f32_16x16x32_bf16 v[110:113], v[162:165], v[226:229], v[110:113]
	v_mfma_f32_16x16x32_bf16 v[106:109], v[186:189], v[226:229], v[106:109]
	s_waitcnt lgkmcnt(1)
	v_mfma_f32_16x16x32_bf16 v[98:101], v[186:189], v[234:237], v[98:101]
	v_mfma_f32_16x16x32_bf16 v[102:105], v[162:165], v[234:237], v[102:105]
	v_mfma_f32_16x16x32_bf16 v[126:129], v[182:185], v[214:217], v[126:129]
	v_mfma_f32_16x16x32_bf16 v[122:125], v[190:193], v[214:217], v[122:125]
	v_mfma_f32_16x16x32_bf16 v[114:117], v[190:193], v[222:225], v[114:117]
	v_mfma_f32_16x16x32_bf16 v[118:121], v[182:185], v[222:225], v[118:121]
	v_mfma_f32_16x16x32_bf16 v[110:113], v[182:185], v[230:233], v[110:113]
	v_mfma_f32_16x16x32_bf16 v[106:109], v[190:193], v[230:233], v[106:109]
	s_waitcnt lgkmcnt(0)
	v_mfma_f32_16x16x32_bf16 v[98:101], v[190:193], v[238:241], v[98:101]
	v_mfma_f32_16x16x32_bf16 v[102:105], v[182:185], v[238:241], v[102:105]
	s_setprio 0
	s_setprio 1
	v_mfma_f32_16x16x32_bf16 v[94:97], v[194:197], v[210:213], v[94:97]
	v_mfma_f32_16x16x32_bf16 v[90:93], v[202:205], v[210:213], v[90:93]
	v_mfma_f32_16x16x32_bf16 v[82:85], v[202:205], v[218:221], v[82:85]
	v_mfma_f32_16x16x32_bf16 v[86:89], v[194:197], v[218:221], v[86:89]
	v_mfma_f32_16x16x32_bf16 v[78:81], v[194:197], v[226:229], v[78:81]
	v_mfma_f32_16x16x32_bf16 v[74:77], v[202:205], v[226:229], v[74:77]
	v_mfma_f32_16x16x32_bf16 v[66:69], v[202:205], v[234:237], v[66:69]
	v_mfma_f32_16x16x32_bf16 v[70:73], v[194:197], v[234:237], v[70:73]
	v_mfma_f32_16x16x32_bf16 v[94:97], v[198:201], v[214:217], v[94:97]
	v_mfma_f32_16x16x32_bf16 v[90:93], v[206:209], v[214:217], v[90:93]
	v_mfma_f32_16x16x32_bf16 v[82:85], v[206:209], v[222:225], v[82:85]
	v_mfma_f32_16x16x32_bf16 v[86:89], v[198:201], v[222:225], v[86:89]
	v_mfma_f32_16x16x32_bf16 v[78:81], v[198:201], v[230:233], v[78:81]
	v_mfma_f32_16x16x32_bf16 v[74:77], v[206:209], v[230:233], v[74:77]
	v_mfma_f32_16x16x32_bf16 v[66:69], v[206:209], v[238:241], v[66:69]
	v_mfma_f32_16x16x32_bf16 v[70:73], v[198:201], v[238:241], v[70:73]
	s_setprio 0
	s_barrier
	s_mov_b32 m0, s37
	s_mov_b32 s10, s6
	s_mov_b32 s11, s7
	ds_read_b128 v[210:213], v180 offset:16384
	ds_read_b128 v[214:217], v180 offset:17408
	ds_read_b128 v[218:221], v180 offset:18432
	ds_read_b128 v[222:225], v180 offset:19456
	ds_read_b128 v[226:229], v180 offset:20480
	ds_read_b128 v[230:233], v180 offset:21504
	ds_read_b128 v[234:237], v180 offset:22528
	ds_read_b128 v[238:241], v180 offset:23552
	buffer_load_dwordx4 v174, s[8:11], s27 offen lds
	s_mov_b32 m0, s38
	s_add_i32 s66, s27, 0x80000
	buffer_load_dwordx4 v176, s[8:11], s27 offen lds
	s_mov_b32 m0, s39
	s_nop 0
	buffer_load_dwordx4 v174, s[8:11], s66 offen lds
	s_mov_b32 m0, s41
	s_nop 0
	buffer_load_dwordx4 v176, s[8:11], s66 offen lds
	s_mov_b32 m0, s36
	s_nop 0
	buffer_load_dwordx4 v1, s[4:7], s29 offen lds
	s_mov_b32 m0, s42
	s_nop 0
	buffer_load_dwordx4 v175, s[4:7], s29 offen lds
	s_waitcnt vmcnt(8)
	s_waitcnt lgkmcnt(0)
	s_barrier
	s_setprio 1
	s_waitcnt lgkmcnt(7)
	v_mfma_f32_16x16x32_bf16 v[62:65], v[162:165], v[210:213], v[62:65]
	v_mfma_f32_16x16x32_bf16 v[58:61], v[186:189], v[210:213], v[58:61]
	s_waitcnt lgkmcnt(5)
	v_mfma_f32_16x16x32_bf16 v[50:53], v[186:189], v[218:221], v[50:53]
	v_mfma_f32_16x16x32_bf16 v[54:57], v[162:165], v[218:221], v[54:57]
	s_waitcnt lgkmcnt(3)
	v_mfma_f32_16x16x32_bf16 v[46:49], v[162:165], v[226:229], v[46:49]
	v_mfma_f32_16x16x32_bf16 v[42:45], v[186:189], v[226:229], v[42:45]
	s_waitcnt lgkmcnt(1)
	v_mfma_f32_16x16x32_bf16 v[34:37], v[186:189], v[234:237], v[34:37]
	v_mfma_f32_16x16x32_bf16 v[38:41], v[162:165], v[234:237], v[38:41]
	v_mfma_f32_16x16x32_bf16 v[62:65], v[182:185], v[214:217], v[62:65]
	v_mfma_f32_16x16x32_bf16 v[58:61], v[190:193], v[214:217], v[58:61]
	v_mfma_f32_16x16x32_bf16 v[50:53], v[190:193], v[222:225], v[50:53]
	v_mfma_f32_16x16x32_bf16 v[54:57], v[182:185], v[222:225], v[54:57]
	v_mfma_f32_16x16x32_bf16 v[46:49], v[182:185], v[230:233], v[46:49]
	v_mfma_f32_16x16x32_bf16 v[42:45], v[190:193], v[230:233], v[42:45]
	s_waitcnt lgkmcnt(0)
	v_mfma_f32_16x16x32_bf16 v[34:37], v[190:193], v[238:241], v[34:37]
	v_mfma_f32_16x16x32_bf16 v[38:41], v[182:185], v[238:241], v[38:41]
	s_setprio 0
	s_setprio 1
	v_mfma_f32_16x16x32_bf16 v[30:33], v[194:197], v[210:213], v[30:33]
	v_mfma_f32_16x16x32_bf16 v[26:29], v[202:205], v[210:213], v[26:29]
	v_mfma_f32_16x16x32_bf16 v[18:21], v[202:205], v[218:221], v[18:21]
	v_mfma_f32_16x16x32_bf16 v[22:25], v[194:197], v[218:221], v[22:25]
	v_mfma_f32_16x16x32_bf16 v[14:17], v[194:197], v[226:229], v[14:17]
	v_mfma_f32_16x16x32_bf16 v[10:13], v[202:205], v[226:229], v[10:13]
	v_mfma_f32_16x16x32_bf16 v[2:5], v[202:205], v[234:237], v[2:5]
	v_mfma_f32_16x16x32_bf16 v[6:9], v[194:197], v[234:237], v[6:9]
	v_mfma_f32_16x16x32_bf16 v[30:33], v[198:201], v[214:217], v[30:33]
	v_mfma_f32_16x16x32_bf16 v[26:29], v[206:209], v[214:217], v[26:29]
	v_mfma_f32_16x16x32_bf16 v[18:21], v[206:209], v[222:225], v[18:21]
	v_mfma_f32_16x16x32_bf16 v[22:25], v[198:201], v[222:225], v[22:25]
	v_mfma_f32_16x16x32_bf16 v[14:17], v[198:201], v[230:233], v[14:17]
	v_mfma_f32_16x16x32_bf16 v[10:13], v[206:209], v[230:233], v[10:13]
	v_mfma_f32_16x16x32_bf16 v[2:5], v[206:209], v[238:241], v[2:5]
	v_mfma_f32_16x16x32_bf16 v[6:9], v[198:201], v[238:241], v[6:9]
	s_setprio 0
	s_barrier
	v_add_u32_e32 v166, 0x18000, v179
	ds_read_b128 v[162:165], v166
	ds_read_b128 v[182:185], v166 offset:1024
	ds_read_b128 v[186:189], v166 offset:2048
	ds_read_b128 v[190:193], v166 offset:3072
	v_add_u32_e32 v166, 0x1c000, v179
	ds_read_b128 v[194:197], v166
	ds_read_b128 v[198:201], v166 offset:1024
	ds_read_b128 v[202:205], v166 offset:2048
	ds_read_b128 v[206:209], v166 offset:3072
	s_add_i32 s29, s29, 0x80000
	s_mov_b32 m0, s43
	ds_read_b128 v[210:213], v180 offset:32768
	ds_read_b128 v[214:217], v180 offset:33792
	ds_read_b128 v[218:221], v180 offset:34816
	ds_read_b128 v[222:225], v180 offset:35840
	ds_read_b128 v[226:229], v180 offset:36864
	ds_read_b128 v[230:233], v180 offset:37888
	ds_read_b128 v[234:237], v180 offset:38912
	ds_read_b128 v[238:241], v180 offset:39936
	buffer_load_dwordx4 v1, s[4:7], s29 offen lds
	s_mov_b32 m0, s44
	s_nop 0
	buffer_load_dwordx4 v175, s[4:7], s29 offen lds
	s_waitcnt vmcnt(8)
	s_waitcnt lgkmcnt(0)
	s_barrier
	s_setprio 1
	s_waitcnt lgkmcnt(7)
	v_mfma_f32_16x16x32_bf16 v[126:129], v[162:165], v[210:213], v[126:129]
	v_mfma_f32_16x16x32_bf16 v[122:125], v[186:189], v[210:213], v[122:125]
	s_waitcnt lgkmcnt(5)
	v_mfma_f32_16x16x32_bf16 v[114:117], v[186:189], v[218:221], v[114:117]
	v_mfma_f32_16x16x32_bf16 v[118:121], v[162:165], v[218:221], v[118:121]
	s_waitcnt lgkmcnt(3)
	v_mfma_f32_16x16x32_bf16 v[110:113], v[162:165], v[226:229], v[110:113]
	v_mfma_f32_16x16x32_bf16 v[106:109], v[186:189], v[226:229], v[106:109]
	s_waitcnt lgkmcnt(1)
	v_mfma_f32_16x16x32_bf16 v[98:101], v[186:189], v[234:237], v[98:101]
	v_mfma_f32_16x16x32_bf16 v[102:105], v[162:165], v[234:237], v[102:105]
	v_mfma_f32_16x16x32_bf16 v[126:129], v[182:185], v[214:217], v[126:129]
	v_mfma_f32_16x16x32_bf16 v[122:125], v[190:193], v[214:217], v[122:125]
	v_mfma_f32_16x16x32_bf16 v[114:117], v[190:193], v[222:225], v[114:117]
	v_mfma_f32_16x16x32_bf16 v[118:121], v[182:185], v[222:225], v[118:121]
	v_mfma_f32_16x16x32_bf16 v[110:113], v[182:185], v[230:233], v[110:113]
	v_mfma_f32_16x16x32_bf16 v[106:109], v[190:193], v[230:233], v[106:109]
	s_waitcnt lgkmcnt(0)
	v_mfma_f32_16x16x32_bf16 v[98:101], v[190:193], v[238:241], v[98:101]
	v_mfma_f32_16x16x32_bf16 v[102:105], v[182:185], v[238:241], v[102:105]
	s_setprio 0
	s_setprio 1
	v_mfma_f32_16x16x32_bf16 v[94:97], v[194:197], v[210:213], v[94:97]
	v_mfma_f32_16x16x32_bf16 v[90:93], v[202:205], v[210:213], v[90:93]
	v_mfma_f32_16x16x32_bf16 v[82:85], v[202:205], v[218:221], v[82:85]
	v_mfma_f32_16x16x32_bf16 v[86:89], v[194:197], v[218:221], v[86:89]
	v_mfma_f32_16x16x32_bf16 v[78:81], v[194:197], v[226:229], v[78:81]
	v_mfma_f32_16x16x32_bf16 v[74:77], v[202:205], v[226:229], v[74:77]
	v_mfma_f32_16x16x32_bf16 v[66:69], v[202:205], v[234:237], v[66:69]
	v_mfma_f32_16x16x32_bf16 v[70:73], v[194:197], v[234:237], v[70:73]
	v_mfma_f32_16x16x32_bf16 v[94:97], v[198:201], v[214:217], v[94:97]
	v_mfma_f32_16x16x32_bf16 v[90:93], v[206:209], v[214:217], v[90:93]
	v_mfma_f32_16x16x32_bf16 v[82:85], v[206:209], v[222:225], v[82:85]
	v_mfma_f32_16x16x32_bf16 v[86:89], v[198:201], v[222:225], v[86:89]
	v_mfma_f32_16x16x32_bf16 v[78:81], v[198:201], v[230:233], v[78:81]
	v_mfma_f32_16x16x32_bf16 v[74:77], v[206:209], v[230:233], v[74:77]
	v_mfma_f32_16x16x32_bf16 v[66:69], v[206:209], v[238:241], v[66:69]
	v_mfma_f32_16x16x32_bf16 v[70:73], v[198:201], v[238:241], v[70:73]
	s_setprio 0
	s_barrier
	s_mov_b32 m0, s49
	ds_read_b128 v[210:213], v180 offset:49152
	ds_read_b128 v[214:217], v180 offset:50176
	ds_read_b128 v[218:221], v180 offset:51200
	ds_read_b128 v[222:225], v180 offset:52224
	ds_read_b128 v[226:229], v180 offset:53248
	ds_read_b128 v[230:233], v180 offset:54272
	ds_read_b128 v[234:237], v180 offset:55296
	ds_read_b128 v[238:241], v180 offset:56320
	buffer_load_dwordx4 v174, s[8:11], s28 offen lds
	s_mov_b32 m0, s50
	s_add_i32 s27, s27, 0x80080
	buffer_load_dwordx4 v176, s[8:11], s28 offen lds
	s_mov_b32 m0, s53
	s_nop 0
	buffer_load_dwordx4 v174, s[8:11], s27 offen lds
	s_mov_b32 m0, s54
	s_nop 0
	buffer_load_dwordx4 v176, s[8:11], s27 offen lds
	s_mov_b32 m0, s51
	s_nop 0
	buffer_load_dwordx4 v1, s[4:7], s26 offen lds
	s_mov_b32 m0, s52
	s_nop 0
	buffer_load_dwordx4 v175, s[4:7], s26 offen lds
	s_waitcnt vmcnt(8)
	s_waitcnt lgkmcnt(0)
	s_barrier
	s_setprio 1
	s_waitcnt lgkmcnt(7)
	v_mfma_f32_16x16x32_bf16 v[62:65], v[162:165], v[210:213], v[62:65]
	v_mfma_f32_16x16x32_bf16 v[58:61], v[186:189], v[210:213], v[58:61]
	s_waitcnt lgkmcnt(5)
	v_mfma_f32_16x16x32_bf16 v[50:53], v[186:189], v[218:221], v[50:53]
	v_mfma_f32_16x16x32_bf16 v[54:57], v[162:165], v[218:221], v[54:57]
	s_waitcnt lgkmcnt(3)
	v_mfma_f32_16x16x32_bf16 v[46:49], v[162:165], v[226:229], v[46:49]
	v_mfma_f32_16x16x32_bf16 v[42:45], v[186:189], v[226:229], v[42:45]
	s_waitcnt lgkmcnt(1)
	v_mfma_f32_16x16x32_bf16 v[34:37], v[186:189], v[234:237], v[34:37]
	v_mfma_f32_16x16x32_bf16 v[38:41], v[162:165], v[234:237], v[38:41]
	v_mfma_f32_16x16x32_bf16 v[62:65], v[182:185], v[214:217], v[62:65]
	v_mfma_f32_16x16x32_bf16 v[58:61], v[190:193], v[214:217], v[58:61]
	v_mfma_f32_16x16x32_bf16 v[50:53], v[190:193], v[222:225], v[50:53]
	v_mfma_f32_16x16x32_bf16 v[54:57], v[182:185], v[222:225], v[54:57]
	v_mfma_f32_16x16x32_bf16 v[46:49], v[182:185], v[230:233], v[46:49]
	v_mfma_f32_16x16x32_bf16 v[42:45], v[190:193], v[230:233], v[42:45]
	s_waitcnt lgkmcnt(0)
	v_mfma_f32_16x16x32_bf16 v[34:37], v[190:193], v[238:241], v[34:37]
	v_mfma_f32_16x16x32_bf16 v[38:41], v[182:185], v[238:241], v[38:41]
	s_setprio 0
	s_setprio 1
	v_mfma_f32_16x16x32_bf16 v[30:33], v[194:197], v[210:213], v[30:33]
	v_mfma_f32_16x16x32_bf16 v[26:29], v[202:205], v[210:213], v[26:29]
	v_mfma_f32_16x16x32_bf16 v[18:21], v[202:205], v[218:221], v[18:21]
	v_mfma_f32_16x16x32_bf16 v[22:25], v[194:197], v[218:221], v[22:25]
	v_mfma_f32_16x16x32_bf16 v[14:17], v[194:197], v[226:229], v[14:17]
	v_mfma_f32_16x16x32_bf16 v[10:13], v[202:205], v[226:229], v[10:13]
	v_mfma_f32_16x16x32_bf16 v[2:5], v[202:205], v[234:237], v[2:5]
	v_mfma_f32_16x16x32_bf16 v[6:9], v[194:197], v[234:237], v[6:9]
	v_mfma_f32_16x16x32_bf16 v[30:33], v[198:201], v[214:217], v[30:33]
	v_mfma_f32_16x16x32_bf16 v[26:29], v[206:209], v[214:217], v[26:29]
	v_mfma_f32_16x16x32_bf16 v[18:21], v[206:209], v[222:225], v[18:21]
	v_mfma_f32_16x16x32_bf16 v[22:25], v[198:201], v[222:225], v[22:25]
	v_mfma_f32_16x16x32_bf16 v[14:17], v[198:201], v[230:233], v[14:17]
	v_mfma_f32_16x16x32_bf16 v[10:13], v[206:209], v[230:233], v[10:13]
	v_mfma_f32_16x16x32_bf16 v[2:5], v[206:209], v[238:241], v[2:5]
	v_mfma_f32_16x16x32_bf16 v[6:9], v[198:201], v[238:241], v[6:9]
	s_setprio 0
	s_barrier
	s_add_i32 s10, s65, 2
	s_addk_i32 s64, 0x100
	s_cmp_gt_u32 s65, 29
	s_cbranch_scc1 .LBB0_910
	s_mov_b32 s65, s10
	s_branch .LBB0_869

.LBB0_1029:
	v_add_u32_e32 v152, 0x10000, v138
	v_add_u32_e32 v168, 0x14000, v138
	ds_read_b128 v[140:143], v152
	ds_read_b128 v[144:147], v152 offset:1024
	ds_read_b128 v[148:151], v152 offset:2048
	ds_read_b128 v[152:155], v152 offset:3072
	ds_read_b128 v[156:159], v168
	ds_read_b128 v[160:163], v168 offset:1024
	ds_read_b128 v[164:167], v168 offset:2048
	ds_read_b128 v[168:171], v168 offset:3072
	s_add_i32 s10, s30, s50
	s_add_i32 s51, s25, s50
	s_add_i32 s11, s10, 0x4000
	s_addk_i32 s51, 0x4000
	s_cmp_eq_u32 s50, 0
	s_cselect_b32 s53, s47, s11
	s_cselect_b32 s52, s48, s51
	s_or_b32 s51, s53, 0x80
	s_add_i32 s10, s10, 0x203f80
	s_mov_b32 m0, s41
	ds_read_b128 v[172:175], v139
	ds_read_b128 v[176:179], v139 offset:1024
	ds_read_b128 v[180:183], v139 offset:2048
	ds_read_b128 v[184:187], v139 offset:3072
	ds_read_b128 v[188:191], v139 offset:4096
	ds_read_b128 v[192:195], v139 offset:5120
	ds_read_b128 v[196:199], v139 offset:6144
	ds_read_b128 v[200:203], v139 offset:7168
	buffer_load_dwordx4 v134, s[4:7], s10 offen lds
	s_mov_b32 m0, s42
	s_nop 0
	buffer_load_dwordx4 v136, s[4:7], s10 offen lds
	s_waitcnt vmcnt(8)
	s_waitcnt lgkmcnt(0)
	s_barrier
	s_setprio 1
	s_waitcnt lgkmcnt(7)
	v_mfma_f32_16x16x32_bf16 v[126:129], v[140:143], v[172:175], v[126:129]
	v_mfma_f32_16x16x32_bf16 v[122:125], v[148:151], v[172:175], v[122:125]
	s_waitcnt lgkmcnt(5)
	v_mfma_f32_16x16x32_bf16 v[106:109], v[148:151], v[180:183], v[106:109]
	v_mfma_f32_16x16x32_bf16 v[114:117], v[140:143], v[180:183], v[114:117]
	s_waitcnt lgkmcnt(3)
	v_mfma_f32_16x16x32_bf16 v[98:101], v[140:143], v[188:191], v[98:101]
	v_mfma_f32_16x16x32_bf16 v[90:93], v[148:151], v[188:191], v[90:93]
	s_waitcnt lgkmcnt(1)
	v_mfma_f32_16x16x32_bf16 v[74:77], v[148:151], v[196:199], v[74:77]
	v_mfma_f32_16x16x32_bf16 v[82:85], v[140:143], v[196:199], v[82:85]
	v_mfma_f32_16x16x32_bf16 v[126:129], v[144:147], v[176:179], v[126:129]
	v_mfma_f32_16x16x32_bf16 v[122:125], v[152:155], v[176:179], v[122:125]
	v_mfma_f32_16x16x32_bf16 v[106:109], v[152:155], v[184:187], v[106:109]
	v_mfma_f32_16x16x32_bf16 v[114:117], v[144:147], v[184:187], v[114:117]
	v_mfma_f32_16x16x32_bf16 v[98:101], v[144:147], v[192:195], v[98:101]
	v_mfma_f32_16x16x32_bf16 v[90:93], v[152:155], v[192:195], v[90:93]
	s_waitcnt lgkmcnt(0)
	v_mfma_f32_16x16x32_bf16 v[74:77], v[152:155], v[200:203], v[74:77]
	v_mfma_f32_16x16x32_bf16 v[82:85], v[144:147], v[200:203], v[82:85]
	s_setprio 0
	s_setprio 1
	v_mfma_f32_16x16x32_bf16 v[118:121], v[156:159], v[172:175], v[118:121]
	v_mfma_f32_16x16x32_bf16 v[110:113], v[164:167], v[172:175], v[110:113]
	v_mfma_f32_16x16x32_bf16 v[94:97], v[164:167], v[180:183], v[94:97]
	v_mfma_f32_16x16x32_bf16 v[102:105], v[156:159], v[180:183], v[102:105]
	v_mfma_f32_16x16x32_bf16 v[86:89], v[156:159], v[188:191], v[86:89]
	v_mfma_f32_16x16x32_bf16 v[78:81], v[164:167], v[188:191], v[78:81]
	v_mfma_f32_16x16x32_bf16 v[66:69], v[164:167], v[196:199], v[66:69]
	v_mfma_f32_16x16x32_bf16 v[70:73], v[156:159], v[196:199], v[70:73]
	v_mfma_f32_16x16x32_bf16 v[118:121], v[160:163], v[176:179], v[118:121]
	v_mfma_f32_16x16x32_bf16 v[110:113], v[168:171], v[176:179], v[110:113]
	v_mfma_f32_16x16x32_bf16 v[94:97], v[168:171], v[184:187], v[94:97]
	v_mfma_f32_16x16x32_bf16 v[102:105], v[160:163], v[184:187], v[102:105]
	v_mfma_f32_16x16x32_bf16 v[86:89], v[160:163], v[192:195], v[86:89]
	v_mfma_f32_16x16x32_bf16 v[78:81], v[168:171], v[192:195], v[78:81]
	v_mfma_f32_16x16x32_bf16 v[66:69], v[168:171], v[200:203], v[66:69]
	v_mfma_f32_16x16x32_bf16 v[70:73], v[160:163], v[200:203], v[70:73]
	s_setprio 0
	s_barrier
	s_mov_b32 m0, s24
	s_mov_b32 s10, s6
	s_mov_b32 s11, s7
	ds_read_b128 v[172:175], v139 offset:16384
	ds_read_b128 v[176:179], v139 offset:17408
	ds_read_b128 v[180:183], v139 offset:18432
	ds_read_b128 v[184:187], v139 offset:19456
	ds_read_b128 v[188:191], v139 offset:20480
	ds_read_b128 v[192:195], v139 offset:21504
	ds_read_b128 v[196:199], v139 offset:22528
	ds_read_b128 v[200:203], v139 offset:23552
	buffer_load_dwordx4 v135, s[8:11], s52 offen lds
	s_mov_b32 m0, s26
	s_add_i32 s54, s52, 0x200000
	buffer_load_dwordx4 v137, s[8:11], s52 offen lds
	s_mov_b32 m0, s27
	s_nop 0
	buffer_load_dwordx4 v135, s[8:11], s54 offen lds
	s_mov_b32 m0, s28
	s_nop 0
	buffer_load_dwordx4 v137, s[8:11], s54 offen lds
	s_mov_b32 m0, s23
	s_nop 0
	buffer_load_dwordx4 v134, s[4:7], s53 offen lds
	s_mov_b32 m0, s29
	s_nop 0
	buffer_load_dwordx4 v136, s[4:7], s53 offen lds
	s_waitcnt vmcnt(8)
	s_waitcnt lgkmcnt(0)
	s_barrier
	s_setprio 1
	s_waitcnt lgkmcnt(7)
	v_mfma_f32_16x16x32_bf16 v[62:65], v[140:143], v[172:175], v[62:65]
	v_mfma_f32_16x16x32_bf16 v[58:61], v[148:151], v[172:175], v[58:61]
	s_waitcnt lgkmcnt(5)
	v_mfma_f32_16x16x32_bf16 v[42:45], v[148:151], v[180:183], v[42:45]
	v_mfma_f32_16x16x32_bf16 v[50:53], v[140:143], v[180:183], v[50:53]
	s_waitcnt lgkmcnt(3)
	v_mfma_f32_16x16x32_bf16 v[34:37], v[140:143], v[188:191], v[34:37]
	v_mfma_f32_16x16x32_bf16 v[26:29], v[148:151], v[188:191], v[26:29]
	s_waitcnt lgkmcnt(1)
	v_mfma_f32_16x16x32_bf16 v[10:13], v[148:151], v[196:199], v[10:13]
	v_mfma_f32_16x16x32_bf16 v[18:21], v[140:143], v[196:199], v[18:21]
	v_mfma_f32_16x16x32_bf16 v[62:65], v[144:147], v[176:179], v[62:65]
	v_mfma_f32_16x16x32_bf16 v[58:61], v[152:155], v[176:179], v[58:61]
	v_mfma_f32_16x16x32_bf16 v[42:45], v[152:155], v[184:187], v[42:45]
	v_mfma_f32_16x16x32_bf16 v[50:53], v[144:147], v[184:187], v[50:53]
	v_mfma_f32_16x16x32_bf16 v[34:37], v[144:147], v[192:195], v[34:37]
	v_mfma_f32_16x16x32_bf16 v[26:29], v[152:155], v[192:195], v[26:29]
	s_waitcnt lgkmcnt(0)
	v_mfma_f32_16x16x32_bf16 v[10:13], v[152:155], v[200:203], v[10:13]
	v_mfma_f32_16x16x32_bf16 v[18:21], v[144:147], v[200:203], v[18:21]
	s_setprio 0
	s_setprio 1
	v_mfma_f32_16x16x32_bf16 v[54:57], v[156:159], v[172:175], v[54:57]
	v_mfma_f32_16x16x32_bf16 v[46:49], v[164:167], v[172:175], v[46:49]
	v_mfma_f32_16x16x32_bf16 v[30:33], v[164:167], v[180:183], v[30:33]
	v_mfma_f32_16x16x32_bf16 v[38:41], v[156:159], v[180:183], v[38:41]
	v_mfma_f32_16x16x32_bf16 v[22:25], v[156:159], v[188:191], v[22:25]
	v_mfma_f32_16x16x32_bf16 v[14:17], v[164:167], v[188:191], v[14:17]
	v_mfma_f32_16x16x32_bf16 v[2:5], v[164:167], v[196:199], v[2:5]
	v_mfma_f32_16x16x32_bf16 v[6:9], v[156:159], v[196:199], v[6:9]
	v_mfma_f32_16x16x32_bf16 v[54:57], v[160:163], v[176:179], v[54:57]
	v_mfma_f32_16x16x32_bf16 v[46:49], v[168:171], v[176:179], v[46:49]
	v_mfma_f32_16x16x32_bf16 v[30:33], v[168:171], v[184:187], v[30:33]
	v_mfma_f32_16x16x32_bf16 v[38:41], v[160:163], v[184:187], v[38:41]
	v_mfma_f32_16x16x32_bf16 v[22:25], v[160:163], v[192:195], v[22:25]
	v_mfma_f32_16x16x32_bf16 v[14:17], v[168:171], v[192:195], v[14:17]
	v_mfma_f32_16x16x32_bf16 v[2:5], v[168:171], v[200:203], v[2:5]
	v_mfma_f32_16x16x32_bf16 v[6:9], v[160:163], v[200:203], v[6:9]
	s_setprio 0
	s_barrier
	v_add_u32_e32 v152, 0x18000, v138
	v_add_u32_e32 v168, 0x1c000, v138
	ds_read_b128 v[140:143], v152
	ds_read_b128 v[144:147], v152 offset:1024
	ds_read_b128 v[148:151], v152 offset:2048
	ds_read_b128 v[152:155], v152 offset:3072
	ds_read_b128 v[156:159], v168
	ds_read_b128 v[160:163], v168 offset:1024
	ds_read_b128 v[164:167], v168 offset:2048
	ds_read_b128 v[168:171], v168 offset:3072
	s_add_i32 s53, s53, 0x200000
	s_mov_b32 m0, s31
	ds_read_b128 v[172:175], v139 offset:32768
	ds_read_b128 v[176:179], v139 offset:33792
	ds_read_b128 v[180:183], v139 offset:34816
	ds_read_b128 v[184:187], v139 offset:35840
	ds_read_b128 v[188:191], v139 offset:36864
	ds_read_b128 v[192:195], v139 offset:37888
	ds_read_b128 v[196:199], v139 offset:38912
	ds_read_b128 v[200:203], v139 offset:39936
	buffer_load_dwordx4 v134, s[4:7], s53 offen lds
	s_mov_b32 m0, s33
	s_nop 0
	buffer_load_dwordx4 v136, s[4:7], s53 offen lds
	s_waitcnt vmcnt(8)
	s_waitcnt lgkmcnt(0)
	s_barrier
	s_setprio 1
	s_waitcnt lgkmcnt(7)
	v_mfma_f32_16x16x32_bf16 v[126:129], v[140:143], v[172:175], v[126:129]
	v_mfma_f32_16x16x32_bf16 v[122:125], v[148:151], v[172:175], v[122:125]
	s_waitcnt lgkmcnt(5)
	v_mfma_f32_16x16x32_bf16 v[106:109], v[148:151], v[180:183], v[106:109]
	v_mfma_f32_16x16x32_bf16 v[114:117], v[140:143], v[180:183], v[114:117]
	s_waitcnt lgkmcnt(3)
	v_mfma_f32_16x16x32_bf16 v[98:101], v[140:143], v[188:191], v[98:101]
	v_mfma_f32_16x16x32_bf16 v[90:93], v[148:151], v[188:191], v[90:93]
	s_waitcnt lgkmcnt(1)
	v_mfma_f32_16x16x32_bf16 v[74:77], v[148:151], v[196:199], v[74:77]
	v_mfma_f32_16x16x32_bf16 v[82:85], v[140:143], v[196:199], v[82:85]
	v_mfma_f32_16x16x32_bf16 v[126:129], v[144:147], v[176:179], v[126:129]
	v_mfma_f32_16x16x32_bf16 v[122:125], v[152:155], v[176:179], v[122:125]
	v_mfma_f32_16x16x32_bf16 v[106:109], v[152:155], v[184:187], v[106:109]
	v_mfma_f32_16x16x32_bf16 v[114:117], v[144:147], v[184:187], v[114:117]
	v_mfma_f32_16x16x32_bf16 v[98:101], v[144:147], v[192:195], v[98:101]
	v_mfma_f32_16x16x32_bf16 v[90:93], v[152:155], v[192:195], v[90:93]
	s_waitcnt lgkmcnt(0)
	v_mfma_f32_16x16x32_bf16 v[74:77], v[152:155], v[200:203], v[74:77]
	v_mfma_f32_16x16x32_bf16 v[82:85], v[144:147], v[200:203], v[82:85]
	s_setprio 0
	s_setprio 1
	v_mfma_f32_16x16x32_bf16 v[118:121], v[156:159], v[172:175], v[118:121]
	v_mfma_f32_16x16x32_bf16 v[110:113], v[164:167], v[172:175], v[110:113]
	v_mfma_f32_16x16x32_bf16 v[94:97], v[164:167], v[180:183], v[94:97]
	v_mfma_f32_16x16x32_bf16 v[102:105], v[156:159], v[180:183], v[102:105]
	v_mfma_f32_16x16x32_bf16 v[86:89], v[156:159], v[188:191], v[86:89]
	v_mfma_f32_16x16x32_bf16 v[78:81], v[164:167], v[188:191], v[78:81]
	v_mfma_f32_16x16x32_bf16 v[66:69], v[164:167], v[196:199], v[66:69]
	v_mfma_f32_16x16x32_bf16 v[70:73], v[156:159], v[196:199], v[70:73]
	v_mfma_f32_16x16x32_bf16 v[118:121], v[160:163], v[176:179], v[118:121]
	v_mfma_f32_16x16x32_bf16 v[110:113], v[168:171], v[176:179], v[110:113]
	v_mfma_f32_16x16x32_bf16 v[94:97], v[168:171], v[184:187], v[94:97]
	v_mfma_f32_16x16x32_bf16 v[102:105], v[160:163], v[184:187], v[102:105]
	v_mfma_f32_16x16x32_bf16 v[86:89], v[160:163], v[192:195], v[86:89]
	v_mfma_f32_16x16x32_bf16 v[78:81], v[168:171], v[192:195], v[78:81]
	v_mfma_f32_16x16x32_bf16 v[66:69], v[168:171], v[200:203], v[66:69]
	v_mfma_f32_16x16x32_bf16 v[70:73], v[160:163], v[200:203], v[70:73]
	s_setprio 0
	s_barrier
	s_mov_b32 m0, s34
	s_or_b32 s53, s52, 0x80
	ds_read_b128 v[172:175], v139 offset:49152
	ds_read_b128 v[176:179], v139 offset:50176
	ds_read_b128 v[180:183], v139 offset:51200
	ds_read_b128 v[184:187], v139 offset:52224
	ds_read_b128 v[188:191], v139 offset:53248
	ds_read_b128 v[192:195], v139 offset:54272
	ds_read_b128 v[196:199], v139 offset:55296
	ds_read_b128 v[200:203], v139 offset:56320
	buffer_load_dwordx4 v135, s[8:11], s53 offen lds
	s_mov_b32 m0, s35
	s_add_i32 s52, s52, 0x200080
	buffer_load_dwordx4 v137, s[8:11], s53 offen lds
	s_mov_b32 m0, s39
	s_nop 0
	buffer_load_dwordx4 v135, s[8:11], s52 offen lds
	s_mov_b32 m0, s40
	s_nop 0
	buffer_load_dwordx4 v137, s[8:11], s52 offen lds
	s_mov_b32 m0, s37
	s_nop 0
	buffer_load_dwordx4 v134, s[4:7], s51 offen lds
	s_mov_b32 m0, s38
	s_nop 0
	buffer_load_dwordx4 v136, s[4:7], s51 offen lds
	s_waitcnt vmcnt(8)
	s_waitcnt lgkmcnt(0)
	s_barrier
	s_setprio 1
	s_waitcnt lgkmcnt(7)
	v_mfma_f32_16x16x32_bf16 v[62:65], v[140:143], v[172:175], v[62:65]
	v_mfma_f32_16x16x32_bf16 v[58:61], v[148:151], v[172:175], v[58:61]
	s_waitcnt lgkmcnt(5)
	v_mfma_f32_16x16x32_bf16 v[42:45], v[148:151], v[180:183], v[42:45]
	v_mfma_f32_16x16x32_bf16 v[50:53], v[140:143], v[180:183], v[50:53]
	s_waitcnt lgkmcnt(3)
	v_mfma_f32_16x16x32_bf16 v[34:37], v[140:143], v[188:191], v[34:37]
	v_mfma_f32_16x16x32_bf16 v[26:29], v[148:151], v[188:191], v[26:29]
	s_waitcnt lgkmcnt(1)
	v_mfma_f32_16x16x32_bf16 v[10:13], v[148:151], v[196:199], v[10:13]
	v_mfma_f32_16x16x32_bf16 v[18:21], v[140:143], v[196:199], v[18:21]
	v_mfma_f32_16x16x32_bf16 v[62:65], v[144:147], v[176:179], v[62:65]
	v_mfma_f32_16x16x32_bf16 v[58:61], v[152:155], v[176:179], v[58:61]
	v_mfma_f32_16x16x32_bf16 v[42:45], v[152:155], v[184:187], v[42:45]
	v_mfma_f32_16x16x32_bf16 v[50:53], v[144:147], v[184:187], v[50:53]
	v_mfma_f32_16x16x32_bf16 v[34:37], v[144:147], v[192:195], v[34:37]
	v_mfma_f32_16x16x32_bf16 v[26:29], v[152:155], v[192:195], v[26:29]
	s_waitcnt lgkmcnt(0)
	v_mfma_f32_16x16x32_bf16 v[10:13], v[152:155], v[200:203], v[10:13]
	v_mfma_f32_16x16x32_bf16 v[18:21], v[144:147], v[200:203], v[18:21]
	s_setprio 0
	s_setprio 1
	v_mfma_f32_16x16x32_bf16 v[54:57], v[156:159], v[172:175], v[54:57]
	v_mfma_f32_16x16x32_bf16 v[46:49], v[164:167], v[172:175], v[46:49]
	v_mfma_f32_16x16x32_bf16 v[30:33], v[164:167], v[180:183], v[30:33]
	v_mfma_f32_16x16x32_bf16 v[38:41], v[156:159], v[180:183], v[38:41]
	v_mfma_f32_16x16x32_bf16 v[22:25], v[156:159], v[188:191], v[22:25]
	v_mfma_f32_16x16x32_bf16 v[14:17], v[164:167], v[188:191], v[14:17]
	v_mfma_f32_16x16x32_bf16 v[2:5], v[164:167], v[196:199], v[2:5]
	v_mfma_f32_16x16x32_bf16 v[6:9], v[156:159], v[196:199], v[6:9]
	v_mfma_f32_16x16x32_bf16 v[54:57], v[160:163], v[176:179], v[54:57]
	v_mfma_f32_16x16x32_bf16 v[46:49], v[168:171], v[176:179], v[46:49]
	v_mfma_f32_16x16x32_bf16 v[30:33], v[168:171], v[184:187], v[30:33]
	v_mfma_f32_16x16x32_bf16 v[38:41], v[160:163], v[184:187], v[38:41]
	v_mfma_f32_16x16x32_bf16 v[22:25], v[160:163], v[192:195], v[22:25]
	v_mfma_f32_16x16x32_bf16 v[14:17], v[168:171], v[192:195], v[14:17]
	v_mfma_f32_16x16x32_bf16 v[2:5], v[168:171], v[200:203], v[2:5]
	v_mfma_f32_16x16x32_bf16 v[6:9], v[160:163], v[200:203], v[6:9]
	s_setprio 0
	s_barrier
	s_add_i32 s49, s49, 2
	s_addk_i32 s50, 0x100
	s_cmpk_gt_u32 s49, 0x7d
	s_cbranch_scc0 .LBB0_1029
	s_andn2_b64 vcc, exec, s[2:3]
	s_cbranch_vccnz .LBB0_1021
	v_mov_b32_e32 v2, 0
	s_mov_b32 s17, s44
	s_mov_b32 s14, s45
	s_mov_b32 s25, s46
	s_mov_b32 s30, s13
	s_mov_b32 s43, s12
	v_mov_b32_e32 v3, v2
	v_mov_b32_e32 v4, v2
	v_mov_b32_e32 v5, v2
	v_mov_b32_e32 v6, v2
	v_mov_b32_e32 v7, v2
	v_mov_b32_e32 v8, v2
	v_mov_b32_e32 v9, v2
	v_mov_b32_e32 v14, v2
	v_mov_b32_e32 v15, v2
	v_mov_b32_e32 v16, v2
	v_mov_b32_e32 v17, v2
	v_mov_b32_e32 v22, v2
	v_mov_b32_e32 v23, v2
	v_mov_b32_e32 v24, v2
	v_mov_b32_e32 v25, v2
	v_mov_b32_e32 v30, v2
	v_mov_b32_e32 v31, v2
	v_mov_b32_e32 v32, v2
	v_mov_b32_e32 v33, v2
	v_mov_b32_e32 v38, v2
	v_mov_b32_e32 v39, v2
	v_mov_b32_e32 v40, v2
	v_mov_b32_e32 v41, v2
	v_mov_b32_e32 v46, v2
	v_mov_b32_e32 v47, v2
	v_mov_b32_e32 v48, v2
	v_mov_b32_e32 v49, v2
	v_mov_b32_e32 v54, v2
	v_mov_b32_e32 v55, v2
	v_mov_b32_e32 v56, v2
	v_mov_b32_e32 v57, v2
	v_mov_b32_e32 v10, v2
	v_mov_b32_e32 v11, v2
	v_mov_b32_e32 v12, v2
	v_mov_b32_e32 v13, v2
	v_mov_b32_e32 v18, v2
	v_mov_b32_e32 v19, v2
	v_mov_b32_e32 v20, v2
	v_mov_b32_e32 v21, v2
	v_mov_b32_e32 v26, v2
	v_mov_b32_e32 v27, v2
	v_mov_b32_e32 v28, v2
	v_mov_b32_e32 v29, v2
	v_mov_b32_e32 v34, v2
	v_mov_b32_e32 v35, v2
	v_mov_b32_e32 v36, v2
	v_mov_b32_e32 v37, v2
	v_mov_b32_e32 v42, v2
	v_mov_b32_e32 v43, v2
	v_mov_b32_e32 v44, v2
	v_mov_b32_e32 v45, v2
	v_mov_b32_e32 v50, v2
	v_mov_b32_e32 v51, v2
	v_mov_b32_e32 v52, v2
	v_mov_b32_e32 v53, v2
	v_mov_b32_e32 v58, v2
	v_mov_b32_e32 v59, v2
	v_mov_b32_e32 v60, v2
	v_mov_b32_e32 v61, v2
	v_mov_b32_e32 v62, v2
	v_mov_b32_e32 v63, v2
	v_mov_b32_e32 v64, v2
	v_mov_b32_e32 v65, v2
	v_mov_b32_e32 v66, v2
	v_mov_b32_e32 v67, v2
	v_mov_b32_e32 v68, v2
	v_mov_b32_e32 v69, v2
	v_mov_b32_e32 v70, v2
	v_mov_b32_e32 v71, v2
	v_mov_b32_e32 v72, v2
	v_mov_b32_e32 v73, v2
	v_mov_b32_e32 v78, v2
	v_mov_b32_e32 v79, v2
	v_mov_b32_e32 v80, v2
	v_mov_b32_e32 v81, v2
	v_mov_b32_e32 v86, v2
	v_mov_b32_e32 v87, v2
	v_mov_b32_e32 v88, v2
	v_mov_b32_e32 v89, v2
	v_mov_b32_e32 v94, v2
	v_mov_b32_e32 v95, v2
	v_mov_b32_e32 v96, v2
	v_mov_b32_e32 v97, v2
	v_mov_b32_e32 v102, v2
	v_mov_b32_e32 v103, v2
	v_mov_b32_e32 v104, v2
	v_mov_b32_e32 v105, v2
	v_mov_b32_e32 v110, v2
	v_mov_b32_e32 v111, v2
	v_mov_b32_e32 v112, v2
	v_mov_b32_e32 v113, v2
	v_mov_b32_e32 v118, v2
	v_mov_b32_e32 v119, v2
	v_mov_b32_e32 v120, v2
	v_mov_b32_e32 v121, v2
	v_mov_b32_e32 v74, v2
	v_mov_b32_e32 v75, v2
	v_mov_b32_e32 v76, v2
	v_mov_b32_e32 v77, v2
	v_mov_b32_e32 v82, v2
	v_mov_b32_e32 v83, v2
	v_mov_b32_e32 v84, v2
	v_mov_b32_e32 v85, v2
	v_mov_b32_e32 v90, v2
	v_mov_b32_e32 v91, v2
	v_mov_b32_e32 v92, v2
	v_mov_b32_e32 v93, v2
	v_mov_b32_e32 v98, v2
	v_mov_b32_e32 v99, v2
	v_mov_b32_e32 v100, v2
	v_mov_b32_e32 v101, v2
	v_mov_b32_e32 v106, v2
	v_mov_b32_e32 v107, v2
	v_mov_b32_e32 v108, v2
	v_mov_b32_e32 v109, v2
	v_mov_b32_e32 v114, v2
	v_mov_b32_e32 v115, v2
	v_mov_b32_e32 v116, v2
	v_mov_b32_e32 v117, v2
	v_mov_b32_e32 v122, v2
	v_mov_b32_e32 v123, v2
	v_mov_b32_e32 v124, v2
	v_mov_b32_e32 v125, v2
	v_mov_b32_e32 v126, v2
	v_mov_b32_e32 v127, v2
	v_mov_b32_e32 v128, v2
	v_mov_b32_e32 v129, v2
	s_branch .LBB0_1021
